# attention-output GEMM's fused residual+norm epilogue: 32 serialized residual loads software-pipelined one row group ahead; row-scale loads hoisted in P17 epilogue too
# speedup vs baseline: 1.0078x; 1.0035x over previous
.LBB0_697:
	s_lshl_b32 s0, s61, 5
	s_lshl_b32 s21, s26, 8
	s_or_b32 s0, s0, s21
	s_lshl_b32 s60, s20, 8
	v_or_b32_e32 v162, s0, v169
	v_add_u32_e32 v166, s60, v179
	v_mov_b32_e32 v167, 0
	v_readlane_b32 s68, v251, 11
	v_ashrrev_i32_e32 v163, 31, v162
	v_lshlrev_b64 v[164:165], 11, v[166:167]
	v_readlane_b32 s69, v251, 12
	v_lshl_add_u64 v[22:23], v[164:165], 0, v[162:163]
	v_readlane_b32 s70, v251, 13
	v_readlane_b32 s71, v251, 14
	v_readlane_b32 s72, v251, 15
	v_readlane_b32 s73, v251, 16
	s_mov_b64 s[0:1], s[68:69]
	s_nop 15
	s_nop 7
	v_lshl_add_u64 v[30:31], v[22:23], 2, s[0:1]
	s_waitcnt vmcnt(0)
	s_barrier
	global_load_dwordx4 v[18:21], v[30:31], off
	v_mov_b32_e32 v198, v30
	v_mov_b32_e32 v199, v31
	s_brev_b32 s0, 60
	s_mov_b64 s[4:5], s[72:73]
	v_lshl_add_u64 v[180:181], v[22:23], 1, s[22:23]
	v_lshl_add_u64 v[6:7], v[162:163], 2, s[4:5]
	global_load_dwordx4 v[10:13], v[6:7], off offset:16
	global_load_dwordx4 v[14:17], v[6:7], off
	global_load_dwordx4 v[2:5], v[6:7], off offset:528
	s_nop 0
	global_load_dwordx4 v[6:9], v[6:7], off offset:512
	s_mov_b32 s98, 0x0
	s_mov_b32 s99, 0
	v_lshl_add_u64 v[230:231], v[198:199], 0, s[98:99]
	global_load_dwordx4 v[222:225], v[230:231], off offset:16
	global_load_dwordx4 v[226:229], v[230:231], off offset:512
	global_load_dwordx4 v[230:233], v[230:231], off offset:528
	s_mov_b32 s98, 0x20000
	s_mov_b32 s99, 0
	v_lshl_add_u64 v[246:247], v[198:199], 0, s[98:99]
	global_load_dwordx4 v[234:237], v[246:247], off
	global_load_dwordx4 v[238:241], v[246:247], off offset:16
	global_load_dwordx4 v[242:245], v[246:247], off offset:512
	global_load_dwordx4 v[246:249], v[246:247], off offset:528
	s_mov_b64 s[2:3], s[70:71]
	v_cmp_gt_u32_e64 s[2:3], 16, v1
	v_readlane_b32 s74, v251, 17
	v_readlane_b32 s75, v251, 18
	v_readlane_b32 s76, v251, 19
	v_readlane_b32 s77, v251, 20
	v_readlane_b32 s78, v251, 21
	v_readlane_b32 s79, v251, 22
	v_readlane_b32 s80, v251, 23
	v_readlane_b32 s81, v251, 24
	v_readlane_b32 s82, v251, 25
	v_readlane_b32 s83, v251, 26
	s_waitcnt vmcnt(7)
	v_pk_fma_f32 v[24:25], v[160:161], s[0:1], v[20:21] op_sel_hi:[1,0,1]
	v_pk_fma_f32 v[22:23], v[158:159], s[0:1], v[18:19] op_sel_hi:[1,0,1]
	v_cvt_pk_bf16_f32 v19, v24, v25
	v_cvt_pk_bf16_f32 v18, v22, v23
	global_store_dwordx2 v[180:181], v[18:19], off
	v_mul_f32_e32 v158, v25, v25
	v_fmac_f32_e32 v158, v24, v24
	s_waitcnt vmcnt(7)
	v_mov_b32_e32 v18, v222
	v_mov_b32_e32 v19, v223
	v_mov_b32_e32 v20, v224
	v_mov_b32_e32 v21, v225
	v_pk_fma_f32 v[28:29], v[156:157], s[0:1], v[20:21] op_sel_hi:[1,0,1]
	v_pk_fma_f32 v[26:27], v[154:155], s[0:1], v[18:19] op_sel_hi:[1,0,1]
	v_cvt_pk_bf16_f32 v19, v28, v29
	v_cvt_pk_bf16_f32 v18, v26, v27
	global_store_dwordx2 v[180:181], v[18:19], off offset:8
	v_mul_f32_e32 v157, v23, v23
	v_fmac_f32_e32 v157, v22, v22
	v_add_f32_e32 v157, v157, v158
	v_mul_f32_e32 v159, v27, v27
	v_mul_f32_e32 v160, v29, v29
	v_fmac_f32_e32 v159, v26, v26
	v_fmac_f32_e32 v160, v28, v28
	s_waitcnt vmcnt(7)
	v_mov_b32_e32 v18, v226
	v_mov_b32_e32 v19, v227
	v_mov_b32_e32 v20, v228
	v_mov_b32_e32 v21, v229
	v_pk_fma_f32 v[20:21], v[152:153], s[0:1], v[20:21] op_sel_hi:[1,0,1]
	v_pk_fma_f32 v[18:19], v[150:151], s[0:1], v[18:19] op_sel_hi:[1,0,1]
	v_cvt_pk_bf16_f32 v33, v20, v21
	v_cvt_pk_bf16_f32 v32, v18, v19
	global_store_dwordx2 v[180:181], v[32:33], off offset:256
	v_mbcnt_lo_u32_b32 v150, -1, 0
	v_mbcnt_hi_u32_b32 v154, -1, v150
	v_and_b32_e32 v151, 64, v154
	v_xor_b32_e32 v150, 16, v154
	v_add_u32_e32 v156, 64, v151
	v_cmp_lt_i32_e32 vcc, v150, v156
	v_pk_mul_f32 v[152:153], v[14:15], v[22:23]
	s_lshl_b32 s1, s61, 3
	v_cndmask_b32_e32 v150, v154, v150, vcc
	v_lshlrev_b32_e32 v168, 2, v150
	v_pk_mul_f32 v[150:151], v[16:17], v[24:25]
	v_xor_b32_e32 v155, 32, v154
	v_max_f32_e64 v150, |v150|, |v151|
	v_max3_f32 v158, |v152|, |v153|, v150
	v_pk_mul_f32 v[150:151], v[12:13], v[28:29]
	v_pk_mul_f32 v[152:153], v[10:11], v[26:27]
	v_max_f32_e64 v150, |v150|, |v151|
	v_add_f32_e32 v151, v159, v160
	v_max3_f32 v150, |v152|, |v153|, v150
	v_add_f32_e32 v157, v157, v151
	v_max3_f32 v158, v158, 0, v150
	v_pk_mul_f32 v[150:151], v[8:9], v[20:21]
	v_mul_f32_e32 v159, v19, v19
	v_mul_f32_e32 v160, v21, v21
	v_pk_mul_f32 v[152:153], v[6:7], v[18:19]
	v_max_f32_e64 v150, |v150|, |v151|
	v_fmac_f32_e32 v159, v18, v18
	v_fmac_f32_e32 v160, v20, v20
	v_max3_f32 v150, |v152|, |v153|, v150
	v_add_f32_e32 v151, v159, v160
	v_add_f32_e32 v151, v157, v151
	v_cmp_lt_i32_e32 vcc, v155, v156
	s_add_i32 s6, s1, 0
	s_waitcnt vmcnt(7)
	v_mov_b32_e32 v30, v230
	v_mov_b32_e32 v31, v231
	v_mov_b32_e32 v32, v232
	v_mov_b32_e32 v33, v233
	s_mov_b32 s98, 0x40000
	s_mov_b32 s99, 0
	v_lshl_add_u64 v[230:231], v[198:199], 0, s[98:99]
	global_load_dwordx4 v[218:221], v[230:231], off
	global_load_dwordx4 v[222:225], v[230:231], off offset:16
	global_load_dwordx4 v[226:229], v[230:231], off offset:512
	global_load_dwordx4 v[230:233], v[230:231], off offset:528
	v_pk_fma_f32 v[32:33], v[148:149], s[0:1], v[32:33] op_sel_hi:[1,0,1]
	v_pk_fma_f32 v[30:31], v[146:147], s[0:1], v[30:31] op_sel_hi:[1,0,1]
	v_mul_f32_e32 v153, v33, v33
	v_mul_f32_e32 v152, v31, v31
	v_pk_mul_f32 v[146:147], v[4:5], v[32:33]
	v_pk_mul_f32 v[148:149], v[2:3], v[30:31]
	v_fmac_f32_e32 v152, v30, v30
	v_fmac_f32_e32 v153, v32, v32
	v_max_f32_e64 v146, |v146|, |v147|
	v_add_f32_e32 v147, v152, v153
	v_max3_f32 v146, |v148|, |v149|, v146
	v_add_f32_e32 v147, v151, v147
	v_max3_f32 v149, v158, v150, v146
	ds_bpermute_b32 v146, v168, v147
	ds_bpermute_b32 v148, v168, v149
	v_cndmask_b32_e32 v150, v154, v155, vcc
	v_lshlrev_b32_e32 v174, 2, v150
	v_cvt_pk_bf16_f32 v150, v30, v31
	s_waitcnt lgkmcnt(1)
	v_add_f32_e32 v146, v147, v146
	s_waitcnt lgkmcnt(0)
	v_max_f32_e32 v147, v148, v148
	v_max_f32_e32 v147, v149, v147
	ds_bpermute_b32 v148, v174, v146
	ds_bpermute_b32 v149, v174, v147
	v_cvt_pk_bf16_f32 v151, v32, v33
	global_store_dwordx2 v[180:181], v[150:151], off offset:264
	s_and_saveexec_b64 s[4:5], s[2:3]
	s_cbranch_execz .LBB0_699
	s_waitcnt lgkmcnt(1)
	v_add_f32_e32 v146, v146, v148
	s_waitcnt lgkmcnt(0)
	v_max_f32_e32 v148, v149, v149
	v_max_f32_e32 v147, v147, v147
	v_lshl_add_u32 v150, v179, 5, s6
	v_max_f32_e32 v147, v147, v148
	ds_write_b64 v150, v[146:147]
.LBB0_699:
	s_or_b64 exec, exec, s[4:5]
	s_waitcnt lgkmcnt(1)
	v_or_b32_e32 v148, 16, v179
	v_add_u32_e32 v166, s60, v148
	v_lshlrev_b64 v[146:147], 11, v[166:167]
	v_readlane_b32 s68, v251, 11
	v_lshl_add_u64 v[154:155], v[146:147], 0, v[162:163]
	v_readlane_b32 s69, v251, 12
	v_readlane_b32 s70, v251, 13
	v_readlane_b32 s71, v251, 14
	v_lshl_add_u64 v[156:157], v[154:155], 2, s[68:69]
	v_lshl_add_u64 v[154:155], v[154:155], 1, s[22:23]
	v_readlane_b32 s72, v251, 15
	v_readlane_b32 s73, v251, 16
	v_readlane_b32 s74, v251, 17
	v_readlane_b32 s75, v251, 18
	v_readlane_b32 s76, v251, 19
	v_readlane_b32 s77, v251, 20
	v_readlane_b32 s78, v251, 21
	v_readlane_b32 s79, v251, 22
	v_readlane_b32 s80, v251, 23
	v_readlane_b32 s81, v251, 24
	v_readlane_b32 s82, v251, 25
	v_readlane_b32 s83, v251, 26
	s_waitcnt vmcnt(11)
	v_mov_b32_e32 v150, v234
	v_mov_b32_e32 v151, v235
	v_mov_b32_e32 v152, v236
	v_mov_b32_e32 v153, v237
	v_pk_fma_f32 v[112:113], v[112:113], s[0:1], v[152:153] op_sel_hi:[1,0,1]
	v_pk_fma_f32 v[110:111], v[110:111], s[0:1], v[150:151] op_sel_hi:[1,0,1]
	v_cvt_pk_bf16_f32 v151, v112, v113
	v_cvt_pk_bf16_f32 v150, v110, v111
	global_store_dwordx2 v[154:155], v[150:151], off
	s_waitcnt lgkmcnt(0)
	v_mul_f32_e32 v149, v111, v111
	v_mul_f32_e32 v160, v113, v113
	v_pk_mul_f32 v[158:159], v[14:15], v[110:111]
	v_fmac_f32_e32 v149, v110, v110
	v_fmac_f32_e32 v160, v112, v112
	v_add_f32_e32 v149, v149, v160
	s_waitcnt vmcnt(11)
	v_mov_b32_e32 v150, v238
	v_mov_b32_e32 v151, v239
	v_mov_b32_e32 v152, v240
	v_mov_b32_e32 v153, v241
	v_pk_fma_f32 v[116:117], v[116:117], s[0:1], v[152:153] op_sel_hi:[1,0,1]
	v_pk_fma_f32 v[114:115], v[114:115], s[0:1], v[150:151] op_sel_hi:[1,0,1]
	v_cvt_pk_bf16_f32 v151, v116, v117
	v_cvt_pk_bf16_f32 v150, v114, v115
	global_store_dwordx2 v[154:155], v[150:151], off offset:8
	v_mul_f32_e32 v161, v115, v115
	v_mul_f32_e32 v166, v117, v117
	v_fmac_f32_e32 v161, v114, v114
	v_fmac_f32_e32 v166, v116, v116
	s_waitcnt vmcnt(11)
	v_mov_b32_e32 v150, v242
	v_mov_b32_e32 v151, v243
	v_mov_b32_e32 v152, v244
	v_mov_b32_e32 v153, v245
	v_pk_fma_f32 v[104:105], v[104:105], s[0:1], v[152:153] op_sel_hi:[1,0,1]
	v_pk_fma_f32 v[102:103], v[102:103], s[0:1], v[150:151] op_sel_hi:[1,0,1]
	v_cvt_pk_bf16_f32 v151, v104, v105
	v_cvt_pk_bf16_f32 v150, v102, v103
	global_store_dwordx2 v[154:155], v[150:151], off offset:256
	v_pk_mul_f32 v[156:157], v[16:17], v[112:113]
	s_waitcnt vmcnt(11)
	v_mov_b32_e32 v150, v246
	v_mov_b32_e32 v151, v247
	v_mov_b32_e32 v152, v248
	v_mov_b32_e32 v153, v249
	s_mov_b32 s98, 0x60000
	s_mov_b32 s99, 0
	v_lshl_add_u64 v[246:247], v[198:199], 0, s[98:99]
	global_load_dwordx4 v[234:237], v[246:247], off
	global_load_dwordx4 v[238:241], v[246:247], off offset:16
	global_load_dwordx4 v[242:245], v[246:247], off offset:512
	global_load_dwordx4 v[246:249], v[246:247], off offset:528
	v_pk_fma_f32 v[124:125], v[124:125], s[0:1], v[152:153] op_sel_hi:[1,0,1]
	v_max_f32_e64 v156, |v156|, |v157|
	v_max3_f32 v160, |v158|, |v159|, v156
	v_pk_mul_f32 v[156:157], v[12:13], v[116:117]
	v_pk_mul_f32 v[158:159], v[10:11], v[114:115]
	v_max_f32_e64 v156, |v156|, |v157|
	v_add_f32_e32 v157, v161, v166
	v_max3_f32 v156, |v158|, |v159|, v156
	v_mul_f32_e32 v161, v103, v103
	v_mul_f32_e32 v166, v105, v105
	v_add_f32_e32 v149, v149, v157
	v_max3_f32 v160, v160, 0, v156
	v_pk_mul_f32 v[156:157], v[8:9], v[104:105]
	v_fmac_f32_e32 v161, v102, v102
	v_fmac_f32_e32 v166, v104, v104
	v_pk_mul_f32 v[158:159], v[6:7], v[102:103]
	v_max_f32_e64 v156, |v156|, |v157|
	v_add_f32_e32 v157, v161, v166
	v_pk_fma_f32 v[122:123], v[122:123], s[0:1], v[150:151] op_sel_hi:[1,0,1]
	v_pk_mul_f32 v[150:151], v[4:5], v[124:125]
	v_max3_f32 v156, |v158|, |v159|, v156
	v_add_f32_e32 v149, v149, v157
	v_mul_f32_e32 v157, v123, v123
	v_mul_f32_e32 v158, v125, v125
	v_pk_mul_f32 v[152:153], v[2:3], v[122:123]
	v_max_f32_e64 v150, |v150|, |v151|
	v_fmac_f32_e32 v157, v122, v122
	v_fmac_f32_e32 v158, v124, v124
	v_max3_f32 v150, |v152|, |v153|, v150
	v_add_f32_e32 v151, v157, v158
	v_max3_f32 v150, v160, v156, v150
	v_add_f32_e32 v149, v149, v151
	ds_bpermute_b32 v152, v168, v150
	ds_bpermute_b32 v151, v168, v149
	v_cvt_pk_bf16_f32 v156, v122, v123
	v_cvt_pk_bf16_f32 v157, v124, v125
	global_store_dwordx2 v[154:155], v[156:157], off offset:264
	s_waitcnt lgkmcnt(1)
	v_max_f32_e32 v152, v152, v152
	s_waitcnt lgkmcnt(0)
	v_add_f32_e32 v149, v149, v151
	v_max_f32_e32 v150, v150, v152
	ds_bpermute_b32 v151, v174, v149
	ds_bpermute_b32 v152, v174, v150
	s_and_saveexec_b64 s[0:1], s[2:3]
	s_cbranch_execz .LBB0_701
	v_lshl_add_u32 v153, v148, 5, s6
	s_waitcnt lgkmcnt(1)
	v_add_f32_e32 v148, v149, v151
	s_waitcnt lgkmcnt(0)
	v_max_f32_e32 v149, v152, v152
	v_max_f32_e32 v150, v150, v150
	v_max_f32_e32 v149, v150, v149
	ds_write_b64 v153, v[148:149]
.LBB0_701:
	s_or_b64 exec, exec, s[0:1]
	s_waitcnt lgkmcnt(0)
	v_or_b32_e32 v152, 32, v179
	v_add_u32_e32 v150, s60, v152
	v_mov_b32_e32 v151, 0
	v_lshlrev_b64 v[148:149], 11, v[150:151]
	v_readlane_b32 s68, v251, 11
	v_lshl_add_u64 v[158:159], v[148:149], 0, v[162:163]
	v_readlane_b32 s69, v251, 12
	s_brev_b32 s0, 60
	v_readlane_b32 s70, v251, 13
	v_lshl_add_u64 v[160:161], v[158:159], 2, s[68:69]
	v_lshl_add_u64 v[158:159], v[158:159], 1, s[22:23]
	v_readlane_b32 s71, v251, 14
	v_readlane_b32 s72, v251, 15
	v_readlane_b32 s73, v251, 16
	v_readlane_b32 s74, v251, 17
	v_readlane_b32 s75, v251, 18
	v_readlane_b32 s76, v251, 19
	v_readlane_b32 s77, v251, 20
	v_readlane_b32 s78, v251, 21
	v_readlane_b32 s79, v251, 22
	v_readlane_b32 s80, v251, 23
	v_readlane_b32 s81, v251, 24
	v_readlane_b32 s82, v251, 25
	v_readlane_b32 s83, v251, 26
	s_waitcnt vmcnt(12)
	v_mov_b32_e32 v154, v218
	v_mov_b32_e32 v155, v219
	v_mov_b32_e32 v156, v220
	v_mov_b32_e32 v157, v221
	v_pk_fma_f32 v[136:137], v[136:137], s[0:1], v[156:157] op_sel_hi:[1,0,1]
	v_pk_fma_f32 v[134:135], v[134:135], s[0:1], v[154:155] op_sel_hi:[1,0,1]
	v_cvt_pk_bf16_f32 v155, v136, v137
	v_cvt_pk_bf16_f32 v154, v134, v135
	global_store_dwordx2 v[158:159], v[154:155], off
	v_mul_f32_e32 v150, v135, v135
	v_mul_f32_e32 v153, v137, v137
	v_pk_mul_f32 v[166:167], v[14:15], v[134:135]
	v_fmac_f32_e32 v150, v134, v134
	v_fmac_f32_e32 v153, v136, v136
	v_add_f32_e32 v150, v150, v153
	s_waitcnt vmcnt(12)
	v_mov_b32_e32 v154, v222
	v_mov_b32_e32 v155, v223
	v_mov_b32_e32 v156, v224
	v_mov_b32_e32 v157, v225
	v_pk_fma_f32 v[140:141], v[140:141], s[0:1], v[156:157] op_sel_hi:[1,0,1]
	v_pk_fma_f32 v[138:139], v[138:139], s[0:1], v[154:155] op_sel_hi:[1,0,1]
	v_cvt_pk_bf16_f32 v155, v140, v141
	v_cvt_pk_bf16_f32 v154, v138, v139
	global_store_dwordx2 v[158:159], v[154:155], off offset:8
	v_mul_f32_e32 v178, v139, v139
	v_mul_f32_e32 v180, v141, v141
	v_fmac_f32_e32 v178, v138, v138
	v_fmac_f32_e32 v180, v140, v140
	s_waitcnt vmcnt(12)
	v_mov_b32_e32 v154, v226
	v_mov_b32_e32 v155, v227
	v_mov_b32_e32 v156, v228
	v_mov_b32_e32 v157, v229
	v_pk_fma_f32 v[132:133], v[132:133], s[0:1], v[156:157] op_sel_hi:[1,0,1]
	v_pk_fma_f32 v[130:131], v[130:131], s[0:1], v[154:155] op_sel_hi:[1,0,1]
	v_cvt_pk_bf16_f32 v155, v132, v133
	v_cvt_pk_bf16_f32 v154, v130, v131
	global_store_dwordx2 v[158:159], v[154:155], off offset:256
	v_pk_mul_f32 v[160:161], v[16:17], v[136:137]
	s_waitcnt vmcnt(12)
	v_mov_b32_e32 v154, v230
	v_mov_b32_e32 v155, v231
	v_mov_b32_e32 v156, v232
	v_mov_b32_e32 v157, v233
	s_mov_b32 s98, 0x100000
	s_mov_b32 s99, 0
	v_lshl_add_u64 v[230:231], v[198:199], 0, s[98:99]
	global_load_dwordx4 v[218:221], v[230:231], off
	global_load_dwordx4 v[222:225], v[230:231], off offset:16
	global_load_dwordx4 v[226:229], v[230:231], off offset:512
	global_load_dwordx4 v[230:233], v[230:231], off offset:528
	v_pk_fma_f32 v[144:145], v[144:145], s[0:1], v[156:157] op_sel_hi:[1,0,1]
	v_max_f32_e64 v160, |v160|, |v161|
	v_max3_f32 v153, |v166|, |v167|, v160
	v_pk_mul_f32 v[160:161], v[12:13], v[140:141]
	v_pk_mul_f32 v[166:167], v[10:11], v[138:139]
	v_max_f32_e64 v160, |v160|, |v161|
	v_add_f32_e32 v161, v178, v180
	v_max3_f32 v160, |v166|, |v167|, v160
	v_mul_f32_e32 v178, v131, v131
	v_mul_f32_e32 v180, v133, v133
	v_add_f32_e32 v150, v150, v161
	v_max3_f32 v153, v153, 0, v160
	v_pk_mul_f32 v[160:161], v[8:9], v[132:133]
	v_fmac_f32_e32 v178, v130, v130
	v_fmac_f32_e32 v180, v132, v132
	v_pk_mul_f32 v[166:167], v[6:7], v[130:131]
	v_max_f32_e64 v160, |v160|, |v161|
	v_add_f32_e32 v161, v178, v180
	v_pk_fma_f32 v[142:143], v[142:143], s[0:1], v[154:155] op_sel_hi:[1,0,1]
	v_pk_mul_f32 v[154:155], v[4:5], v[144:145]
	v_max3_f32 v160, |v166|, |v167|, v160
	v_add_f32_e32 v150, v150, v161
	v_mul_f32_e32 v161, v143, v143
	v_mul_f32_e32 v166, v145, v145
	v_pk_mul_f32 v[156:157], v[2:3], v[142:143]
	v_max_f32_e64 v154, |v154|, |v155|
	v_fmac_f32_e32 v161, v142, v142
	v_fmac_f32_e32 v166, v144, v144
	v_max3_f32 v154, |v156|, |v157|, v154
	v_add_f32_e32 v155, v161, v166
	v_max3_f32 v153, v153, v160, v154
	v_add_f32_e32 v150, v150, v155
	ds_bpermute_b32 v155, v168, v153
	ds_bpermute_b32 v154, v168, v150
	v_cvt_pk_bf16_f32 v156, v142, v143
	v_cvt_pk_bf16_f32 v157, v144, v145
	global_store_dwordx2 v[158:159], v[156:157], off offset:264
	s_waitcnt lgkmcnt(1)
	v_max_f32_e32 v155, v155, v155
	s_waitcnt lgkmcnt(0)
	v_add_f32_e32 v150, v150, v154
	v_max_f32_e32 v153, v153, v155
	ds_bpermute_b32 v154, v174, v150
	ds_bpermute_b32 v155, v174, v153
	s_and_saveexec_b64 s[4:5], s[2:3]
	s_cbranch_execz .LBB0_703
	v_lshl_add_u32 v156, v152, 5, s6
	s_waitcnt lgkmcnt(1)
	v_add_f32_e32 v152, v150, v154
	s_waitcnt lgkmcnt(0)
	v_max_f32_e32 v150, v155, v155
	v_max_f32_e32 v153, v153, v153
	v_max_f32_e32 v153, v153, v150
	ds_write_b64 v156, v[152:153]
.LBB0_703:
	s_or_b64 exec, exec, s[4:5]
	v_or_b32_e32 v152, 48, v179
	v_add_u32_e32 v150, s60, v152
	v_lshlrev_b64 v[150:151], 11, v[150:151]
	v_readlane_b32 s68, v251, 11
	v_lshl_add_u64 v[158:159], v[150:151], 0, v[162:163]
	v_readlane_b32 s69, v251, 12
	v_readlane_b32 s70, v251, 13
	v_readlane_b32 s71, v251, 14
	v_lshl_add_u64 v[160:161], v[158:159], 2, s[68:69]
	s_waitcnt lgkmcnt(0)
	v_lshl_add_u64 v[158:159], v[158:159], 1, s[22:23]
	v_readlane_b32 s72, v251, 15
	v_readlane_b32 s73, v251, 16
	v_readlane_b32 s74, v251, 17
	v_readlane_b32 s75, v251, 18
	v_readlane_b32 s76, v251, 19
	v_readlane_b32 s77, v251, 20
	v_readlane_b32 s78, v251, 21
	v_readlane_b32 s79, v251, 22
	v_readlane_b32 s80, v251, 23
	v_readlane_b32 s81, v251, 24
	v_readlane_b32 s82, v251, 25
	v_readlane_b32 s83, v251, 26
	s_waitcnt vmcnt(12)
	v_mov_b32_e32 v154, v234
	v_mov_b32_e32 v155, v235
	v_mov_b32_e32 v156, v236
	v_mov_b32_e32 v157, v237
	v_pk_fma_f32 v[128:129], v[128:129], s[0:1], v[156:157] op_sel_hi:[1,0,1]
	v_pk_fma_f32 v[126:127], v[126:127], s[0:1], v[154:155] op_sel_hi:[1,0,1]
	v_cvt_pk_bf16_f32 v155, v128, v129
	v_cvt_pk_bf16_f32 v154, v126, v127
	global_store_dwordx2 v[158:159], v[154:155], off
	v_mul_f32_e32 v153, v127, v127
	v_mul_f32_e32 v178, v129, v129
	v_pk_mul_f32 v[166:167], v[14:15], v[126:127]
	v_fmac_f32_e32 v153, v126, v126
	v_fmac_f32_e32 v178, v128, v128
	v_add_f32_e32 v153, v153, v178
	s_waitcnt vmcnt(12)
	v_mov_b32_e32 v154, v238
	v_mov_b32_e32 v155, v239
	v_mov_b32_e32 v156, v240
	v_mov_b32_e32 v157, v241
	v_pk_fma_f32 v[120:121], v[120:121], s[0:1], v[156:157] op_sel_hi:[1,0,1]
	v_pk_fma_f32 v[118:119], v[118:119], s[0:1], v[154:155] op_sel_hi:[1,0,1]
	v_cvt_pk_bf16_f32 v155, v120, v121
	v_cvt_pk_bf16_f32 v154, v118, v119
	global_store_dwordx2 v[158:159], v[154:155], off offset:8
	v_mul_f32_e32 v180, v119, v119
	v_mul_f32_e32 v181, v121, v121
	v_fmac_f32_e32 v180, v118, v118
	v_fmac_f32_e32 v181, v120, v120
	s_waitcnt vmcnt(12)
	v_mov_b32_e32 v154, v242
	v_mov_b32_e32 v155, v243
	v_mov_b32_e32 v156, v244
	v_mov_b32_e32 v157, v245
	v_pk_fma_f32 v[108:109], v[108:109], s[0:1], v[156:157] op_sel_hi:[1,0,1]
	v_pk_fma_f32 v[106:107], v[106:107], s[0:1], v[154:155] op_sel_hi:[1,0,1]
	v_cvt_pk_bf16_f32 v155, v108, v109
	v_cvt_pk_bf16_f32 v154, v106, v107
	global_store_dwordx2 v[158:159], v[154:155], off offset:256
	v_pk_mul_f32 v[160:161], v[16:17], v[128:129]
	s_waitcnt vmcnt(12)
	v_mov_b32_e32 v154, v246
	v_mov_b32_e32 v155, v247
	v_mov_b32_e32 v156, v248
	v_mov_b32_e32 v157, v249
	s_mov_b32 s98, 0x120000
	s_mov_b32 s99, 0
	v_lshl_add_u64 v[246:247], v[198:199], 0, s[98:99]
	global_load_dwordx4 v[234:237], v[246:247], off
	global_load_dwordx4 v[238:241], v[246:247], off offset:16
	global_load_dwordx4 v[242:245], v[246:247], off offset:512
	global_load_dwordx4 v[246:249], v[246:247], off offset:528
	v_pk_fma_f32 v[100:101], v[100:101], s[0:1], v[156:157] op_sel_hi:[1,0,1]
	v_max_f32_e64 v160, |v160|, |v161|
	v_max3_f32 v178, |v166|, |v167|, v160
	v_pk_mul_f32 v[160:161], v[12:13], v[120:121]
	v_pk_mul_f32 v[166:167], v[10:11], v[118:119]
	v_max_f32_e64 v160, |v160|, |v161|
	v_add_f32_e32 v161, v180, v181
	v_max3_f32 v160, |v166|, |v167|, v160
	v_mul_f32_e32 v180, v107, v107
	v_mul_f32_e32 v181, v109, v109
	v_add_f32_e32 v153, v153, v161
	v_max3_f32 v178, v178, 0, v160
	v_pk_mul_f32 v[160:161], v[8:9], v[108:109]
	v_fmac_f32_e32 v180, v106, v106
	v_fmac_f32_e32 v181, v108, v108
	v_pk_mul_f32 v[166:167], v[6:7], v[106:107]
	v_max_f32_e64 v160, |v160|, |v161|
	v_add_f32_e32 v161, v180, v181
	v_pk_fma_f32 v[98:99], v[98:99], s[0:1], v[154:155] op_sel_hi:[1,0,1]
	v_pk_mul_f32 v[154:155], v[4:5], v[100:101]
	v_max3_f32 v160, |v166|, |v167|, v160
	v_add_f32_e32 v153, v153, v161
	v_mul_f32_e32 v161, v99, v99
	v_mul_f32_e32 v166, v101, v101
	v_pk_mul_f32 v[156:157], v[2:3], v[98:99]
	v_max_f32_e64 v154, |v154|, |v155|
	v_fmac_f32_e32 v161, v98, v98
	v_fmac_f32_e32 v166, v100, v100
	v_max3_f32 v154, |v156|, |v157|, v154
	v_add_f32_e32 v155, v161, v166
	v_max3_f32 v154, v178, v160, v154
	v_add_f32_e32 v153, v153, v155
	ds_bpermute_b32 v156, v168, v154
	ds_bpermute_b32 v155, v168, v153
	v_cvt_pk_bf16_f32 v160, v98, v99
	v_cvt_pk_bf16_f32 v161, v100, v101
	global_store_dwordx2 v[158:159], v[160:161], off offset:264
	s_waitcnt lgkmcnt(1)
	v_max_f32_e32 v156, v156, v156
	s_waitcnt lgkmcnt(0)
	v_add_f32_e32 v153, v153, v155
	v_max_f32_e32 v154, v154, v156
	ds_bpermute_b32 v155, v174, v153
	ds_bpermute_b32 v156, v174, v154
	s_and_saveexec_b64 s[0:1], s[2:3]
	s_cbranch_execz .LBB0_705
	v_lshl_add_u32 v157, v152, 5, s6
	s_waitcnt lgkmcnt(1)
	v_add_f32_e32 v152, v153, v155
	s_waitcnt lgkmcnt(0)
	v_max_f32_e32 v153, v156, v156
	v_max_f32_e32 v154, v154, v154
	v_max_f32_e32 v153, v154, v153
	ds_write_b64 v157, v[152:153]
.LBB0_705:
	s_or_b64 exec, exec, s[0:1]
	s_waitcnt lgkmcnt(0)
	v_add_u32_e32 v156, 0x80, v179
	v_add_u32_e32 v154, s60, v156
	v_mov_b32_e32 v155, 0
	v_lshlrev_b64 v[152:153], 11, v[154:155]
	v_readlane_b32 s68, v251, 11
	v_lshl_add_u64 v[166:167], v[152:153], 0, v[162:163]
	v_readlane_b32 s69, v251, 12
	s_brev_b32 s0, 60
	v_readlane_b32 s70, v251, 13
	v_lshl_add_u64 v[180:181], v[166:167], 2, s[68:69]
	v_lshl_add_u64 v[166:167], v[166:167], 1, s[22:23]
	v_readlane_b32 s71, v251, 14
	v_readlane_b32 s72, v251, 15
	v_readlane_b32 s73, v251, 16
	v_readlane_b32 s74, v251, 17
	v_readlane_b32 s75, v251, 18
	v_readlane_b32 s76, v251, 19
	v_readlane_b32 s77, v251, 20
	v_readlane_b32 s78, v251, 21
	v_readlane_b32 s79, v251, 22
	v_readlane_b32 s80, v251, 23
	v_readlane_b32 s81, v251, 24
	v_readlane_b32 s82, v251, 25
	v_readlane_b32 s83, v251, 26
	s_waitcnt vmcnt(12)
	v_mov_b32_e32 v158, v218
	v_mov_b32_e32 v159, v219
	v_mov_b32_e32 v160, v220
	v_mov_b32_e32 v161, v221
	v_pk_fma_f32 v[96:97], v[96:97], s[0:1], v[160:161] op_sel_hi:[1,0,1]
	v_pk_fma_f32 v[94:95], v[94:95], s[0:1], v[158:159] op_sel_hi:[1,0,1]
	v_cvt_pk_bf16_f32 v159, v96, v97
	v_cvt_pk_bf16_f32 v158, v94, v95
	global_store_dwordx2 v[166:167], v[158:159], off
	v_mul_f32_e32 v154, v95, v95
	v_mul_f32_e32 v157, v97, v97
	v_pk_mul_f32 v[182:183], v[14:15], v[94:95]
	v_fmac_f32_e32 v154, v94, v94
	v_fmac_f32_e32 v157, v96, v96
	v_add_f32_e32 v154, v154, v157
	s_waitcnt vmcnt(12)
	v_mov_b32_e32 v158, v222
	v_mov_b32_e32 v159, v223
	v_mov_b32_e32 v160, v224
	v_mov_b32_e32 v161, v225
	v_pk_fma_f32 v[92:93], v[92:93], s[0:1], v[160:161] op_sel_hi:[1,0,1]
	v_pk_fma_f32 v[90:91], v[90:91], s[0:1], v[158:159] op_sel_hi:[1,0,1]
	v_cvt_pk_bf16_f32 v159, v92, v93
	v_cvt_pk_bf16_f32 v158, v90, v91
	global_store_dwordx2 v[166:167], v[158:159], off offset:8
	v_mul_f32_e32 v184, v93, v93
	v_fmac_f32_e32 v184, v92, v92
	s_waitcnt vmcnt(12)
	v_mov_b32_e32 v158, v226
	v_mov_b32_e32 v159, v227
	v_mov_b32_e32 v160, v228
	v_mov_b32_e32 v161, v229
	v_pk_fma_f32 v[88:89], v[88:89], s[0:1], v[160:161] op_sel_hi:[1,0,1]
	v_pk_fma_f32 v[86:87], v[86:87], s[0:1], v[158:159] op_sel_hi:[1,0,1]
	v_cvt_pk_bf16_f32 v159, v88, v89
	v_cvt_pk_bf16_f32 v158, v86, v87
	global_store_dwordx2 v[166:167], v[158:159], off offset:256
	v_pk_mul_f32 v[180:181], v[16:17], v[96:97]
	s_waitcnt vmcnt(12)
	v_mov_b32_e32 v158, v230
	v_mov_b32_e32 v159, v231
	v_mov_b32_e32 v160, v232
	v_mov_b32_e32 v161, v233
	s_mov_b32 s98, 0x140000
	s_mov_b32 s99, 0
	v_lshl_add_u64 v[230:231], v[198:199], 0, s[98:99]
	global_load_dwordx4 v[218:221], v[230:231], off
	global_load_dwordx4 v[222:225], v[230:231], off offset:16
	global_load_dwordx4 v[226:229], v[230:231], off offset:512
	global_load_dwordx4 v[230:233], v[230:231], off offset:528
	v_pk_fma_f32 v[84:85], v[84:85], s[0:1], v[160:161] op_sel_hi:[1,0,1]
	v_max_f32_e64 v178, |v180|, |v181|
	v_max3_f32 v157, |v182|, |v183|, v178
	v_mul_f32_e32 v178, v91, v91
	v_fmac_f32_e32 v178, v90, v90
	v_pk_mul_f32 v[180:181], v[12:13], v[92:93]
	v_add_f32_e32 v178, v178, v184
	v_pk_mul_f32 v[182:183], v[10:11], v[90:91]
	v_max_f32_e64 v180, |v180|, |v181|
	v_add_f32_e32 v154, v154, v178
	v_mul_f32_e32 v178, v87, v87
	v_mul_f32_e32 v184, v89, v89
	v_max3_f32 v180, |v182|, |v183|, v180
	v_fmac_f32_e32 v178, v86, v86
	v_fmac_f32_e32 v184, v88, v88
	v_max3_f32 v157, v157, 0, v180
	v_pk_mul_f32 v[180:181], v[8:9], v[88:89]
	v_add_f32_e32 v178, v178, v184
	v_pk_fma_f32 v[82:83], v[82:83], s[0:1], v[158:159] op_sel_hi:[1,0,1]
	v_pk_mul_f32 v[158:159], v[4:5], v[84:85]
	v_pk_mul_f32 v[182:183], v[6:7], v[86:87]
	v_max_f32_e64 v180, |v180|, |v181|
	v_add_f32_e32 v154, v154, v178
	v_mul_f32_e32 v178, v83, v83
	v_mul_f32_e32 v181, v85, v85
	v_pk_mul_f32 v[160:161], v[2:3], v[82:83]
	v_max_f32_e64 v158, |v158|, |v159|
	v_max3_f32 v180, |v182|, |v183|, v180
	v_fmac_f32_e32 v178, v82, v82
	v_fmac_f32_e32 v181, v84, v84
	v_max3_f32 v158, |v160|, |v161|, v158
	v_add_f32_e32 v159, v178, v181
	v_max3_f32 v157, v157, v180, v158
	v_add_f32_e32 v154, v154, v159
	ds_bpermute_b32 v159, v168, v157
	ds_bpermute_b32 v158, v168, v154
	v_cvt_pk_bf16_f32 v160, v82, v83
	v_cvt_pk_bf16_f32 v161, v84, v85
	global_store_dwordx2 v[166:167], v[160:161], off offset:264
	s_waitcnt lgkmcnt(1)
	v_max_f32_e32 v159, v159, v159
	s_waitcnt lgkmcnt(0)
	v_add_f32_e32 v154, v154, v158
	v_max_f32_e32 v157, v157, v159
	ds_bpermute_b32 v158, v174, v154
	ds_bpermute_b32 v159, v174, v157
	s_and_saveexec_b64 s[4:5], s[2:3]
	s_cbranch_execz .LBB0_707
	v_lshl_add_u32 v160, v156, 5, s6
	s_waitcnt lgkmcnt(1)
	v_add_f32_e32 v156, v154, v158
	s_waitcnt lgkmcnt(0)
	v_max_f32_e32 v154, v159, v159
	v_max_f32_e32 v157, v157, v157
	v_max_f32_e32 v157, v157, v154
	ds_write_b64 v160, v[156:157]
.LBB0_707:
	s_or_b64 exec, exec, s[4:5]
	v_add_u32_e32 v156, 0x90, v179
	v_add_u32_e32 v154, s60, v156
	v_lshlrev_b64 v[154:155], 11, v[154:155]
	v_readlane_b32 s68, v251, 11
	v_lshl_add_u64 v[166:167], v[154:155], 0, v[162:163]
	v_readlane_b32 s69, v251, 12
	v_readlane_b32 s70, v251, 13
	v_readlane_b32 s71, v251, 14
	v_lshl_add_u64 v[180:181], v[166:167], 2, s[68:69]
	s_waitcnt lgkmcnt(0)
	v_lshl_add_u64 v[166:167], v[166:167], 1, s[22:23]
	v_readlane_b32 s72, v251, 15
	v_readlane_b32 s73, v251, 16
	v_readlane_b32 s74, v251, 17
	v_readlane_b32 s75, v251, 18
	v_readlane_b32 s76, v251, 19
	v_readlane_b32 s77, v251, 20
	v_readlane_b32 s78, v251, 21
	v_readlane_b32 s79, v251, 22
	v_readlane_b32 s80, v251, 23
	v_readlane_b32 s81, v251, 24
	v_readlane_b32 s82, v251, 25
	v_readlane_b32 s83, v251, 26
	s_waitcnt vmcnt(12)
	v_mov_b32_e32 v158, v234
	v_mov_b32_e32 v159, v235
	v_mov_b32_e32 v160, v236
	v_mov_b32_e32 v161, v237
	v_pk_fma_f32 v[80:81], v[80:81], s[0:1], v[160:161] op_sel_hi:[1,0,1]
	v_pk_fma_f32 v[78:79], v[78:79], s[0:1], v[158:159] op_sel_hi:[1,0,1]
	v_cvt_pk_bf16_f32 v159, v80, v81
	v_cvt_pk_bf16_f32 v158, v78, v79
	global_store_dwordx2 v[166:167], v[158:159], off
	v_mul_f32_e32 v157, v79, v79
	v_mul_f32_e32 v178, v81, v81
	v_pk_mul_f32 v[182:183], v[14:15], v[78:79]
	v_fmac_f32_e32 v157, v78, v78
	v_fmac_f32_e32 v178, v80, v80
	v_add_f32_e32 v157, v157, v178
	s_waitcnt vmcnt(12)
	v_mov_b32_e32 v158, v238
	v_mov_b32_e32 v159, v239
	v_mov_b32_e32 v160, v240
	v_mov_b32_e32 v161, v241
	v_pk_fma_f32 v[76:77], v[76:77], s[0:1], v[160:161] op_sel_hi:[1,0,1]
	v_pk_fma_f32 v[74:75], v[74:75], s[0:1], v[158:159] op_sel_hi:[1,0,1]
	v_cvt_pk_bf16_f32 v159, v76, v77
	v_cvt_pk_bf16_f32 v158, v74, v75
	global_store_dwordx2 v[166:167], v[158:159], off offset:8
	v_mul_f32_e32 v184, v75, v75
	v_mul_f32_e32 v185, v77, v77
	v_fmac_f32_e32 v184, v74, v74
	v_fmac_f32_e32 v185, v76, v76
	s_waitcnt vmcnt(12)
	v_mov_b32_e32 v158, v242
	v_mov_b32_e32 v159, v243
	v_mov_b32_e32 v160, v244
	v_mov_b32_e32 v161, v245
	v_pk_fma_f32 v[72:73], v[72:73], s[0:1], v[160:161] op_sel_hi:[1,0,1]
	v_pk_fma_f32 v[70:71], v[70:71], s[0:1], v[158:159] op_sel_hi:[1,0,1]
	v_cvt_pk_bf16_f32 v159, v72, v73
	v_cvt_pk_bf16_f32 v158, v70, v71
	global_store_dwordx2 v[166:167], v[158:159], off offset:256
	v_pk_mul_f32 v[180:181], v[16:17], v[80:81]
	s_waitcnt vmcnt(12)
	v_mov_b32_e32 v158, v246
	v_mov_b32_e32 v159, v247
	v_mov_b32_e32 v160, v248
	v_mov_b32_e32 v161, v249
	s_mov_b32 s98, 0x160000
	s_mov_b32 s99, 0
	v_lshl_add_u64 v[246:247], v[198:199], 0, s[98:99]
	global_load_dwordx4 v[234:237], v[246:247], off
	global_load_dwordx4 v[238:241], v[246:247], off offset:16
	global_load_dwordx4 v[242:245], v[246:247], off offset:512
	global_load_dwordx4 v[246:249], v[246:247], off offset:528
	v_pk_fma_f32 v[68:69], v[68:69], s[0:1], v[160:161] op_sel_hi:[1,0,1]
	v_max_f32_e64 v180, |v180|, |v181|
	v_max3_f32 v178, |v182|, |v183|, v180
	v_pk_mul_f32 v[180:181], v[12:13], v[76:77]
	v_pk_mul_f32 v[182:183], v[10:11], v[74:75]
	v_max_f32_e64 v180, |v180|, |v181|
	v_add_f32_e32 v181, v184, v185
	v_max3_f32 v180, |v182|, |v183|, v180
	v_mul_f32_e32 v184, v71, v71
	v_mul_f32_e32 v185, v73, v73
	v_add_f32_e32 v157, v157, v181
	v_max3_f32 v178, v178, 0, v180
	v_pk_mul_f32 v[180:181], v[8:9], v[72:73]
	v_fmac_f32_e32 v184, v70, v70
	v_fmac_f32_e32 v185, v72, v72
	v_pk_mul_f32 v[182:183], v[6:7], v[70:71]
	v_max_f32_e64 v180, |v180|, |v181|
	v_add_f32_e32 v181, v184, v185
	v_pk_fma_f32 v[66:67], v[66:67], s[0:1], v[158:159] op_sel_hi:[1,0,1]
	v_pk_mul_f32 v[158:159], v[4:5], v[68:69]
	v_max3_f32 v180, |v182|, |v183|, v180
	v_add_f32_e32 v157, v157, v181
	v_mul_f32_e32 v181, v67, v67
	v_mul_f32_e32 v182, v69, v69
	v_pk_mul_f32 v[160:161], v[2:3], v[66:67]
	v_max_f32_e64 v158, |v158|, |v159|
	v_fmac_f32_e32 v181, v66, v66
	v_fmac_f32_e32 v182, v68, v68
	v_max3_f32 v158, |v160|, |v161|, v158
	v_add_f32_e32 v159, v181, v182
	v_max3_f32 v158, v178, v180, v158
	v_add_f32_e32 v157, v157, v159
	ds_bpermute_b32 v160, v168, v158
	ds_bpermute_b32 v159, v168, v157
	v_cvt_pk_bf16_f32 v180, v66, v67
	v_cvt_pk_bf16_f32 v181, v68, v69
	global_store_dwordx2 v[166:167], v[180:181], off offset:264
	s_waitcnt lgkmcnt(1)
	v_max_f32_e32 v160, v160, v160
	s_waitcnt lgkmcnt(0)
	v_add_f32_e32 v157, v157, v159
	v_max_f32_e32 v158, v158, v160
	ds_bpermute_b32 v159, v174, v157
	ds_bpermute_b32 v160, v174, v158
	s_and_saveexec_b64 s[0:1], s[2:3]
	s_cbranch_execz .LBB0_709
	v_lshl_add_u32 v161, v156, 5, s6
	s_waitcnt lgkmcnt(1)
	v_add_f32_e32 v156, v157, v159
	s_waitcnt lgkmcnt(0)
	v_max_f32_e32 v157, v160, v160
	v_max_f32_e32 v158, v158, v158
	v_max_f32_e32 v157, v158, v157
	ds_write_b64 v161, v[156:157]
.LBB0_709:
	s_or_b64 exec, exec, s[0:1]
	s_waitcnt lgkmcnt(0)
	v_add_u32_e32 v160, 0xa0, v179
	v_add_u32_e32 v158, s60, v160
	v_mov_b32_e32 v159, 0
	v_lshlrev_b64 v[156:157], 11, v[158:159]
	v_readlane_b32 s68, v251, 11
	v_lshl_add_u64 v[166:167], v[156:157], 0, v[162:163]
	v_readlane_b32 s69, v251, 12
	s_brev_b32 s0, 60
	v_lshl_add_u64 v[186:187], v[166:167], 1, s[22:23]
	v_lshl_add_u64 v[184:185], v[166:167], 2, s[68:69]
	v_readlane_b32 s70, v251, 13
	v_readlane_b32 s71, v251, 14
	v_readlane_b32 s72, v251, 15
	v_readlane_b32 s73, v251, 16
	v_readlane_b32 s74, v251, 17
	v_readlane_b32 s75, v251, 18
	v_readlane_b32 s76, v251, 19
	v_readlane_b32 s77, v251, 20
	v_readlane_b32 s78, v251, 21
	v_readlane_b32 s79, v251, 22
	v_readlane_b32 s80, v251, 23
	v_readlane_b32 s81, v251, 24
	v_readlane_b32 s82, v251, 25
	v_readlane_b32 s83, v251, 26
	s_waitcnt vmcnt(12)
	v_mov_b32_e32 v180, v218
	v_mov_b32_e32 v181, v219
	v_mov_b32_e32 v182, v220
	v_mov_b32_e32 v183, v221
	v_pk_fma_f32 v[64:65], v[64:65], s[0:1], v[182:183] op_sel_hi:[1,0,1]
	v_pk_fma_f32 v[62:63], v[62:63], s[0:1], v[180:181] op_sel_hi:[1,0,1]
	v_cvt_pk_bf16_f32 v167, v64, v65
	v_cvt_pk_bf16_f32 v166, v62, v63
	global_store_dwordx2 v[186:187], v[166:167], off
	v_mul_f32_e32 v158, v63, v63
	v_mul_f32_e32 v161, v65, v65
	v_fmac_f32_e32 v158, v62, v62
	v_fmac_f32_e32 v161, v64, v64
	v_add_f32_e32 v158, v158, v161
	s_waitcnt vmcnt(12)
	v_mov_b32_e32 v180, v222
	v_mov_b32_e32 v181, v223
	v_mov_b32_e32 v182, v224
	v_mov_b32_e32 v183, v225
	v_pk_fma_f32 v[60:61], v[60:61], s[0:1], v[182:183] op_sel_hi:[1,0,1]
	v_pk_fma_f32 v[58:59], v[58:59], s[0:1], v[180:181] op_sel_hi:[1,0,1]
	v_cvt_pk_bf16_f32 v167, v60, v61
	v_cvt_pk_bf16_f32 v166, v58, v59
	global_store_dwordx2 v[186:187], v[166:167], off offset:8
	v_mul_f32_e32 v178, v59, v59
	v_mul_f32_e32 v188, v61, v61
	v_fmac_f32_e32 v178, v58, v58
	v_fmac_f32_e32 v188, v60, v60
	s_waitcnt vmcnt(12)
	v_mov_b32_e32 v180, v226
	v_mov_b32_e32 v181, v227
	v_mov_b32_e32 v182, v228
	v_mov_b32_e32 v183, v229
	v_pk_fma_f32 v[56:57], v[56:57], s[0:1], v[182:183] op_sel_hi:[1,0,1]
	v_pk_fma_f32 v[54:55], v[54:55], s[0:1], v[180:181] op_sel_hi:[1,0,1]
	v_cvt_pk_bf16_f32 v167, v56, v57
	v_cvt_pk_bf16_f32 v166, v54, v55
	global_store_dwordx2 v[186:187], v[166:167], off offset:256
	v_pk_mul_f32 v[166:167], v[16:17], v[64:65]
	v_pk_mul_f32 v[184:185], v[14:15], v[62:63]
	v_max_f32_e64 v166, |v166|, |v167|
	v_max3_f32 v161, |v184|, |v185|, v166
	v_pk_mul_f32 v[166:167], v[12:13], v[60:61]
	v_pk_mul_f32 v[184:185], v[10:11], v[58:59]
	v_max_f32_e64 v166, |v166|, |v167|
	v_add_f32_e32 v167, v178, v188
	v_max3_f32 v166, |v184|, |v185|, v166
	v_mul_f32_e32 v178, v55, v55
	v_mul_f32_e32 v188, v57, v57
	v_add_f32_e32 v158, v158, v167
	v_max3_f32 v161, v161, 0, v166
	v_pk_mul_f32 v[166:167], v[8:9], v[56:57]
	v_fmac_f32_e32 v178, v54, v54
	v_fmac_f32_e32 v188, v56, v56
	v_pk_mul_f32 v[184:185], v[6:7], v[54:55]
	v_max_f32_e64 v166, |v166|, |v167|
	v_add_f32_e32 v167, v178, v188
	v_max3_f32 v178, |v184|, |v185|, v166
	v_add_f32_e32 v158, v158, v167
	s_waitcnt vmcnt(12)
	v_mov_b32_e32 v180, v230
	v_mov_b32_e32 v181, v231
	v_mov_b32_e32 v182, v232
	v_mov_b32_e32 v183, v233
	v_pk_fma_f32 v[52:53], v[52:53], s[0:1], v[182:183] op_sel_hi:[1,0,1]
	v_pk_fma_f32 v[50:51], v[50:51], s[0:1], v[180:181] op_sel_hi:[1,0,1]
	v_pk_mul_f32 v[166:167], v[4:5], v[52:53]
	v_mul_f32_e32 v182, v51, v51
	v_mul_f32_e32 v183, v53, v53
	v_pk_mul_f32 v[180:181], v[2:3], v[50:51]
	v_max_f32_e64 v166, |v166|, |v167|
	v_fmac_f32_e32 v182, v50, v50
	v_fmac_f32_e32 v183, v52, v52
	v_max3_f32 v166, |v180|, |v181|, v166
	v_add_f32_e32 v167, v182, v183
	v_max3_f32 v161, v161, v178, v166
	v_add_f32_e32 v158, v158, v167
	ds_bpermute_b32 v167, v168, v161
	ds_bpermute_b32 v166, v168, v158
	v_cvt_pk_bf16_f32 v180, v50, v51
	v_cvt_pk_bf16_f32 v181, v52, v53
	global_store_dwordx2 v[186:187], v[180:181], off offset:264
	s_waitcnt lgkmcnt(1)
	v_max_f32_e32 v167, v167, v167
	s_waitcnt lgkmcnt(0)
	v_add_f32_e32 v158, v158, v166
	v_max_f32_e32 v161, v161, v167
	ds_bpermute_b32 v166, v174, v158
	ds_bpermute_b32 v167, v174, v161
	s_and_saveexec_b64 s[4:5], s[2:3]
	s_cbranch_execz .LBB0_711
	v_lshl_add_u32 v178, v160, 5, s6
	s_waitcnt lgkmcnt(1)
	v_add_f32_e32 v160, v158, v166
	s_waitcnt lgkmcnt(0)
	v_max_f32_e32 v158, v167, v167
	v_max_f32_e32 v161, v161, v161
	v_max_f32_e32 v161, v161, v158
	ds_write_b64 v178, v[160:161]
.LBB0_711:
	s_or_b64 exec, exec, s[4:5]
	v_add_u32_e32 v160, 0xb0, v179
	v_add_u32_e32 v158, s60, v160
	v_lshlrev_b64 v[158:159], 11, v[158:159]
	v_readlane_b32 s68, v251, 11
	s_waitcnt lgkmcnt(0)
	v_lshl_add_u64 v[166:167], v[158:159], 0, v[162:163]
	v_readlane_b32 s69, v251, 12
	v_lshl_add_u64 v[186:187], v[166:167], 1, s[22:23]
	v_readlane_b32 s70, v251, 13
	v_lshl_add_u64 v[184:185], v[166:167], 2, s[68:69]
	v_readlane_b32 s71, v251, 14
	v_readlane_b32 s72, v251, 15
	v_readlane_b32 s73, v251, 16
	v_readlane_b32 s74, v251, 17
	v_readlane_b32 s75, v251, 18
	v_readlane_b32 s76, v251, 19
	v_readlane_b32 s77, v251, 20
	v_readlane_b32 s78, v251, 21
	v_readlane_b32 s79, v251, 22
	v_readlane_b32 s80, v251, 23
	v_readlane_b32 s81, v251, 24
	v_readlane_b32 s82, v251, 25
	v_readlane_b32 s83, v251, 26
	s_waitcnt vmcnt(8)
	v_mov_b32_e32 v180, v234
	v_mov_b32_e32 v181, v235
	v_mov_b32_e32 v182, v236
	v_mov_b32_e32 v183, v237
	v_pk_fma_f32 v[48:49], v[48:49], s[0:1], v[182:183] op_sel_hi:[1,0,1]
	v_pk_fma_f32 v[46:47], v[46:47], s[0:1], v[180:181] op_sel_hi:[1,0,1]
	v_cvt_pk_bf16_f32 v167, v48, v49
	v_cvt_pk_bf16_f32 v166, v46, v47
	global_store_dwordx2 v[186:187], v[166:167], off
	v_mul_f32_e32 v161, v47, v47
	v_mul_f32_e32 v178, v49, v49
	v_fmac_f32_e32 v161, v46, v46
	v_fmac_f32_e32 v178, v48, v48
	v_add_f32_e32 v161, v161, v178
	s_waitcnt vmcnt(8)
	v_mov_b32_e32 v180, v238
	v_mov_b32_e32 v181, v239
	v_mov_b32_e32 v182, v240
	v_mov_b32_e32 v183, v241
	v_pk_fma_f32 v[44:45], v[44:45], s[0:1], v[182:183] op_sel_hi:[1,0,1]
	v_pk_fma_f32 v[42:43], v[42:43], s[0:1], v[180:181] op_sel_hi:[1,0,1]
	v_cvt_pk_bf16_f32 v167, v44, v45
	v_cvt_pk_bf16_f32 v166, v42, v43
	global_store_dwordx2 v[186:187], v[166:167], off offset:8
	v_mul_f32_e32 v188, v43, v43
	v_mul_f32_e32 v189, v45, v45
	v_fmac_f32_e32 v188, v42, v42
	v_fmac_f32_e32 v189, v44, v44
	s_waitcnt vmcnt(8)
	v_mov_b32_e32 v180, v242
	v_mov_b32_e32 v181, v243
	v_mov_b32_e32 v182, v244
	v_mov_b32_e32 v183, v245
	v_pk_fma_f32 v[40:41], v[40:41], s[0:1], v[182:183] op_sel_hi:[1,0,1]
	v_pk_fma_f32 v[38:39], v[38:39], s[0:1], v[180:181] op_sel_hi:[1,0,1]
	v_cvt_pk_bf16_f32 v167, v40, v41
	v_cvt_pk_bf16_f32 v166, v38, v39
	global_store_dwordx2 v[186:187], v[166:167], off offset:256
	v_pk_mul_f32 v[166:167], v[16:17], v[48:49]
	v_pk_mul_f32 v[184:185], v[14:15], v[46:47]
	v_max_f32_e64 v166, |v166|, |v167|
	v_max3_f32 v178, |v184|, |v185|, v166
	v_pk_mul_f32 v[166:167], v[12:13], v[44:45]
	v_pk_mul_f32 v[184:185], v[10:11], v[42:43]
	v_max_f32_e64 v166, |v166|, |v167|
	v_add_f32_e32 v167, v188, v189
	v_max3_f32 v166, |v184|, |v185|, v166
	v_mul_f32_e32 v188, v39, v39
	v_mul_f32_e32 v189, v41, v41
	v_add_f32_e32 v161, v161, v167
	v_max3_f32 v178, v178, 0, v166
	v_pk_mul_f32 v[166:167], v[8:9], v[40:41]
	v_fmac_f32_e32 v188, v38, v38
	v_fmac_f32_e32 v189, v40, v40
	v_pk_mul_f32 v[184:185], v[6:7], v[38:39]
	v_max_f32_e64 v166, |v166|, |v167|
	v_add_f32_e32 v167, v188, v189
	v_max3_f32 v184, |v184|, |v185|, v166
	v_add_f32_e32 v161, v161, v167
	s_waitcnt vmcnt(8)
	v_mov_b32_e32 v180, v246
	v_mov_b32_e32 v181, v247
	v_mov_b32_e32 v182, v248
	v_mov_b32_e32 v183, v249
	v_pk_fma_f32 v[36:37], v[36:37], s[0:1], v[182:183] op_sel_hi:[1,0,1]
	v_pk_fma_f32 v[34:35], v[34:35], s[0:1], v[180:181] op_sel_hi:[1,0,1]
	v_pk_mul_f32 v[166:167], v[4:5], v[36:37]
	v_mul_f32_e32 v182, v35, v35
	v_mul_f32_e32 v183, v37, v37
	v_pk_mul_f32 v[180:181], v[2:3], v[34:35]
	v_max_f32_e64 v166, |v166|, |v167|
	v_fmac_f32_e32 v182, v34, v34
	v_fmac_f32_e32 v183, v36, v36
	v_max3_f32 v166, |v180|, |v181|, v166
	v_add_f32_e32 v167, v182, v183
	v_max3_f32 v166, v178, v184, v166
	v_add_f32_e32 v161, v161, v167
	ds_bpermute_b32 v178, v168, v166
	ds_bpermute_b32 v167, v168, v161
	v_cvt_pk_bf16_f32 v180, v34, v35
	v_cvt_pk_bf16_f32 v181, v36, v37
	global_store_dwordx2 v[186:187], v[180:181], off offset:264
	s_waitcnt lgkmcnt(1)
	v_max_f32_e32 v178, v178, v178
	s_waitcnt lgkmcnt(0)
	v_add_f32_e32 v161, v161, v167
	v_max_f32_e32 v166, v166, v178
	ds_bpermute_b32 v167, v174, v161
	ds_bpermute_b32 v178, v174, v166
	s_and_saveexec_b64 s[0:1], s[2:3]
	s_cbranch_execz .LBB0_713
	v_lshl_add_u32 v180, v160, 5, s6
	s_waitcnt lgkmcnt(1)
	v_add_f32_e32 v160, v161, v167
	s_waitcnt lgkmcnt(0)
	v_max_f32_e32 v161, v178, v178
	v_max_f32_e32 v166, v166, v166
	v_max_f32_e32 v161, v166, v161
	ds_write_b64 v180, v[160:161]

.LBB0_744:
	s_lshl_b32 s0, s20, 5
	s_or_b32 s0, s0, s21
	s_lshl_b32 s10, s60, 8
	v_or_b32_e32 v162, s0, v169
	v_add_u32_e32 v166, s10, v179
	v_mov_b32_e32 v167, 0
	v_readlane_b32 s60, v251, 11
	v_ashrrev_i32_e32 v163, 31, v162
	v_lshlrev_b64 v[164:165], 11, v[166:167]
	v_readlane_b32 s61, v251, 12
	v_lshl_add_u64 v[22:23], v[164:165], 0, v[162:163]
	v_readlane_b32 s62, v251, 13
	v_readlane_b32 s63, v251, 14
	v_readlane_b32 s64, v251, 15
	v_readlane_b32 s65, v251, 16
	s_mov_b64 s[40:41], s[60:61]
	s_nop 15
	s_nop 7
	v_lshl_add_u64 v[30:31], v[22:23], 2, s[40:41]
	s_waitcnt vmcnt(0)
	s_barrier
	global_load_dwordx4 v[18:21], v[30:31], off
	v_mov_b32_e32 v198, v30
	v_mov_b32_e32 v199, v31
	s_brev_b32 s0, 60
	s_mov_b64 s[44:45], s[64:65]
	v_lshl_add_u64 v[170:171], v[22:23], 1, s[22:23]
	v_lshl_add_u64 v[6:7], v[162:163], 2, s[44:45]
	global_load_dwordx4 v[10:13], v[6:7], off offset:16
	global_load_dwordx4 v[14:17], v[6:7], off
	global_load_dwordx4 v[2:5], v[6:7], off offset:528
	s_nop 0
	global_load_dwordx4 v[6:9], v[6:7], off offset:512
	s_mov_b32 s98, 0x0
	s_mov_b32 s99, 0
	v_lshl_add_u64 v[230:231], v[198:199], 0, s[98:99]
	global_load_dwordx4 v[222:225], v[230:231], off offset:16
	global_load_dwordx4 v[226:229], v[230:231], off offset:512
	global_load_dwordx4 v[230:233], v[230:231], off offset:528
	s_mov_b32 s98, 0x20000
	s_mov_b32 s99, 0
	v_lshl_add_u64 v[246:247], v[198:199], 0, s[98:99]
	global_load_dwordx4 v[234:237], v[246:247], off
	global_load_dwordx4 v[238:241], v[246:247], off offset:16
	global_load_dwordx4 v[242:245], v[246:247], off offset:512
	global_load_dwordx4 v[246:249], v[246:247], off offset:528
	v_readlane_b32 s66, v251, 17
	v_readlane_b32 s67, v251, 18
	v_readlane_b32 s68, v251, 19
	v_readlane_b32 s69, v251, 20
	v_readlane_b32 s70, v251, 21
	v_readlane_b32 s71, v251, 22
	v_readlane_b32 s72, v251, 23
	v_readlane_b32 s73, v251, 24
	v_readlane_b32 s74, v251, 25
	v_readlane_b32 s75, v251, 26
	s_mov_b64 s[42:43], s[62:63]
	s_waitcnt vmcnt(7)
	v_pk_fma_f32 v[24:25], v[160:161], s[0:1], v[20:21] op_sel_hi:[1,0,1]
	v_pk_fma_f32 v[22:23], v[158:159], s[0:1], v[18:19] op_sel_hi:[1,0,1]
	v_cvt_pk_bf16_f32 v19, v24, v25
	v_cvt_pk_bf16_f32 v18, v22, v23
	global_store_dwordx2 v[170:171], v[18:19], off
	s_waitcnt vmcnt(7)
	v_mov_b32_e32 v18, v222
	v_mov_b32_e32 v19, v223
	v_mov_b32_e32 v20, v224
	v_mov_b32_e32 v21, v225
	v_pk_fma_f32 v[28:29], v[156:157], s[0:1], v[20:21] op_sel_hi:[1,0,1]
	v_pk_fma_f32 v[26:27], v[154:155], s[0:1], v[18:19] op_sel_hi:[1,0,1]
	v_cvt_pk_bf16_f32 v19, v28, v29
	v_cvt_pk_bf16_f32 v18, v26, v27
	global_store_dwordx2 v[170:171], v[18:19], off offset:8
	v_mul_f32_e32 v154, v23, v23
	v_mul_f32_e32 v155, v25, v25
	v_fmac_f32_e32 v154, v22, v22
	v_fmac_f32_e32 v155, v24, v24
	v_add_f32_e32 v154, v154, v155
	v_mul_f32_e32 v156, v27, v27
	v_mul_f32_e32 v157, v29, v29
	v_fmac_f32_e32 v156, v26, v26
	v_fmac_f32_e32 v157, v28, v28
	s_waitcnt vmcnt(7)
	v_mov_b32_e32 v18, v226
	v_mov_b32_e32 v19, v227
	v_mov_b32_e32 v20, v228
	v_mov_b32_e32 v21, v229
	v_pk_fma_f32 v[20:21], v[152:153], s[0:1], v[20:21] op_sel_hi:[1,0,1]
	v_pk_fma_f32 v[18:19], v[150:151], s[0:1], v[18:19] op_sel_hi:[1,0,1]
	v_cvt_pk_bf16_f32 v33, v20, v21
	v_cvt_pk_bf16_f32 v32, v18, v19
	global_store_dwordx2 v[170:171], v[32:33], off offset:256
	v_pk_mul_f32 v[150:151], v[16:17], v[24:25]
	v_pk_mul_f32 v[152:153], v[14:15], v[22:23]
	v_max_f32_e64 v150, |v150|, |v151|
	v_max3_f32 v155, |v152|, |v153|, v150
	v_pk_mul_f32 v[150:151], v[12:13], v[28:29]
	v_pk_mul_f32 v[152:153], v[10:11], v[26:27]
	v_max_f32_e64 v150, |v150|, |v151|
	v_add_f32_e32 v151, v156, v157
	v_max3_f32 v150, |v152|, |v153|, v150
	v_add_f32_e32 v154, v154, v151
	v_max3_f32 v155, v155, 0, v150
	v_pk_mul_f32 v[150:151], v[8:9], v[20:21]
	v_mul_f32_e32 v156, v19, v19
	v_mul_f32_e32 v157, v21, v21
	v_pk_mul_f32 v[152:153], v[6:7], v[18:19]
	v_max_f32_e64 v150, |v150|, |v151|
	v_fmac_f32_e32 v156, v18, v18
	v_fmac_f32_e32 v157, v20, v20
	v_max3_f32 v150, |v152|, |v153|, v150
	v_add_f32_e32 v151, v156, v157
	v_add_f32_e32 v151, v154, v151
	s_waitcnt vmcnt(7)
	v_mov_b32_e32 v30, v230
	v_mov_b32_e32 v31, v231
	v_mov_b32_e32 v32, v232
	v_mov_b32_e32 v33, v233
	s_mov_b32 s98, 0x40000
	s_mov_b32 s99, 0
	v_lshl_add_u64 v[230:231], v[198:199], 0, s[98:99]
	global_load_dwordx4 v[218:221], v[230:231], off
	global_load_dwordx4 v[222:225], v[230:231], off offset:16
	global_load_dwordx4 v[226:229], v[230:231], off offset:512
	global_load_dwordx4 v[230:233], v[230:231], off offset:528
	v_pk_fma_f32 v[32:33], v[148:149], s[0:1], v[32:33] op_sel_hi:[1,0,1]
	v_pk_fma_f32 v[30:31], v[146:147], s[0:1], v[30:31] op_sel_hi:[1,0,1]
	v_mul_f32_e32 v153, v33, v33
	v_mul_f32_e32 v152, v31, v31
	v_pk_mul_f32 v[146:147], v[4:5], v[32:33]
	v_pk_mul_f32 v[148:149], v[2:3], v[30:31]
	v_fmac_f32_e32 v152, v30, v30
	v_fmac_f32_e32 v153, v32, v32
	v_max_f32_e64 v146, |v146|, |v147|
	v_add_f32_e32 v147, v152, v153
	v_max3_f32 v146, |v148|, |v149|, v146
	v_add_f32_e32 v147, v151, v147
	v_max3_f32 v149, v155, v150, v146
	ds_bpermute_b32 v146, v168, v147
	ds_bpermute_b32 v148, v168, v149
	s_lshl_b32 s1, s20, 3
	s_add_i32 s11, s1, 0
	v_cvt_pk_bf16_f32 v150, v30, v31
	s_waitcnt lgkmcnt(1)
	v_add_f32_e32 v146, v147, v146
	s_waitcnt lgkmcnt(0)
	v_max_f32_e32 v147, v148, v148
	v_max_f32_e32 v147, v149, v147
	ds_bpermute_b32 v148, v174, v146
	ds_bpermute_b32 v149, v174, v147
	v_cvt_pk_bf16_f32 v151, v32, v33
	global_store_dwordx2 v[170:171], v[150:151], off offset:264
	s_and_saveexec_b64 s[14:15], s[2:3]
	s_cbranch_execz .LBB0_746
	s_waitcnt lgkmcnt(1)
	v_add_f32_e32 v146, v146, v148
	s_waitcnt lgkmcnt(0)
	v_max_f32_e32 v148, v149, v149
	v_max_f32_e32 v147, v147, v147
	v_lshl_add_u32 v150, v179, 5, s11
	v_max_f32_e32 v147, v147, v148
	ds_write_b64 v150, v[146:147]
.LBB0_746:
	s_or_b64 exec, exec, s[14:15]
	s_waitcnt lgkmcnt(1)
	v_or_b32_e32 v148, 16, v179
	v_add_u32_e32 v166, s10, v148
	v_lshlrev_b64 v[146:147], 11, v[166:167]
	v_readlane_b32 s60, v251, 11
	v_lshl_add_u64 v[154:155], v[146:147], 0, v[162:163]
	v_readlane_b32 s61, v251, 12
	v_readlane_b32 s62, v251, 13
	v_readlane_b32 s63, v251, 14
	v_lshl_add_u64 v[156:157], v[154:155], 2, s[60:61]
	v_lshl_add_u64 v[154:155], v[154:155], 1, s[22:23]
	v_readlane_b32 s64, v251, 15
	v_readlane_b32 s65, v251, 16
	v_readlane_b32 s66, v251, 17
	v_readlane_b32 s67, v251, 18
	v_readlane_b32 s68, v251, 19
	v_readlane_b32 s69, v251, 20
	v_readlane_b32 s70, v251, 21
	v_readlane_b32 s71, v251, 22
	v_readlane_b32 s72, v251, 23
	v_readlane_b32 s73, v251, 24
	v_readlane_b32 s74, v251, 25
	v_readlane_b32 s75, v251, 26
	s_waitcnt vmcnt(11)
	v_mov_b32_e32 v150, v234
	v_mov_b32_e32 v151, v235
	v_mov_b32_e32 v152, v236
	v_mov_b32_e32 v153, v237
	v_pk_fma_f32 v[108:109], v[108:109], s[0:1], v[152:153] op_sel_hi:[1,0,1]
	v_pk_fma_f32 v[106:107], v[106:107], s[0:1], v[150:151] op_sel_hi:[1,0,1]
	v_cvt_pk_bf16_f32 v151, v108, v109
	v_cvt_pk_bf16_f32 v150, v106, v107
	global_store_dwordx2 v[154:155], v[150:151], off
	s_waitcnt lgkmcnt(0)
	v_mul_f32_e32 v149, v107, v107
	v_mul_f32_e32 v160, v109, v109
	v_pk_mul_f32 v[158:159], v[14:15], v[106:107]
	v_fmac_f32_e32 v149, v106, v106
	v_fmac_f32_e32 v160, v108, v108
	v_add_f32_e32 v149, v149, v160
	s_waitcnt vmcnt(11)
	v_mov_b32_e32 v150, v238
	v_mov_b32_e32 v151, v239
	v_mov_b32_e32 v152, v240
	v_mov_b32_e32 v153, v241
	v_pk_fma_f32 v[112:113], v[112:113], s[0:1], v[152:153] op_sel_hi:[1,0,1]
	v_pk_fma_f32 v[110:111], v[110:111], s[0:1], v[150:151] op_sel_hi:[1,0,1]
	v_cvt_pk_bf16_f32 v151, v112, v113
	v_cvt_pk_bf16_f32 v150, v110, v111
	global_store_dwordx2 v[154:155], v[150:151], off offset:8
	v_mul_f32_e32 v161, v111, v111
	v_mul_f32_e32 v166, v113, v113
	v_fmac_f32_e32 v161, v110, v110
	v_fmac_f32_e32 v166, v112, v112
	s_waitcnt vmcnt(11)
	v_mov_b32_e32 v150, v242
	v_mov_b32_e32 v151, v243
	v_mov_b32_e32 v152, v244
	v_mov_b32_e32 v153, v245
	v_pk_fma_f32 v[104:105], v[104:105], s[0:1], v[152:153] op_sel_hi:[1,0,1]
	v_pk_fma_f32 v[102:103], v[102:103], s[0:1], v[150:151] op_sel_hi:[1,0,1]
	v_cvt_pk_bf16_f32 v151, v104, v105
	v_cvt_pk_bf16_f32 v150, v102, v103
	global_store_dwordx2 v[154:155], v[150:151], off offset:256
	v_pk_mul_f32 v[156:157], v[16:17], v[108:109]
	s_waitcnt vmcnt(11)
	v_mov_b32_e32 v150, v246
	v_mov_b32_e32 v151, v247
	v_mov_b32_e32 v152, v248
	v_mov_b32_e32 v153, v249
	s_mov_b32 s98, 0x60000
	s_mov_b32 s99, 0
	v_lshl_add_u64 v[246:247], v[198:199], 0, s[98:99]
	global_load_dwordx4 v[234:237], v[246:247], off
	global_load_dwordx4 v[238:241], v[246:247], off offset:16
	global_load_dwordx4 v[242:245], v[246:247], off offset:512
	global_load_dwordx4 v[246:249], v[246:247], off offset:528
	v_pk_fma_f32 v[120:121], v[120:121], s[0:1], v[152:153] op_sel_hi:[1,0,1]
	v_max_f32_e64 v156, |v156|, |v157|
	v_max3_f32 v160, |v158|, |v159|, v156
	v_pk_mul_f32 v[156:157], v[12:13], v[112:113]
	v_pk_mul_f32 v[158:159], v[10:11], v[110:111]
	v_max_f32_e64 v156, |v156|, |v157|
	v_add_f32_e32 v157, v161, v166
	v_max3_f32 v156, |v158|, |v159|, v156
	v_mul_f32_e32 v161, v103, v103
	v_mul_f32_e32 v166, v105, v105
	v_add_f32_e32 v149, v149, v157
	v_max3_f32 v160, v160, 0, v156
	v_pk_mul_f32 v[156:157], v[8:9], v[104:105]
	v_fmac_f32_e32 v161, v102, v102
	v_fmac_f32_e32 v166, v104, v104
	v_pk_mul_f32 v[158:159], v[6:7], v[102:103]
	v_max_f32_e64 v156, |v156|, |v157|
	v_add_f32_e32 v157, v161, v166
	v_pk_fma_f32 v[118:119], v[118:119], s[0:1], v[150:151] op_sel_hi:[1,0,1]
	v_pk_mul_f32 v[150:151], v[4:5], v[120:121]
	v_max3_f32 v156, |v158|, |v159|, v156
	v_add_f32_e32 v149, v149, v157
	v_mul_f32_e32 v157, v119, v119
	v_mul_f32_e32 v158, v121, v121
	v_pk_mul_f32 v[152:153], v[2:3], v[118:119]
	v_max_f32_e64 v150, |v150|, |v151|
	v_fmac_f32_e32 v157, v118, v118
	v_fmac_f32_e32 v158, v120, v120
	v_max3_f32 v150, |v152|, |v153|, v150
	v_add_f32_e32 v151, v157, v158
	v_max3_f32 v150, v160, v156, v150
	v_add_f32_e32 v149, v149, v151
	ds_bpermute_b32 v152, v168, v150
	ds_bpermute_b32 v151, v168, v149
	v_cvt_pk_bf16_f32 v156, v118, v119
	v_cvt_pk_bf16_f32 v157, v120, v121
	global_store_dwordx2 v[154:155], v[156:157], off offset:264
	s_waitcnt lgkmcnt(1)
	v_max_f32_e32 v152, v152, v152
	s_waitcnt lgkmcnt(0)
	v_add_f32_e32 v149, v149, v151
	v_max_f32_e32 v150, v150, v152
	ds_bpermute_b32 v151, v174, v149
	ds_bpermute_b32 v152, v174, v150
	s_and_saveexec_b64 s[0:1], s[2:3]
	s_cbranch_execz .LBB0_748
	v_lshl_add_u32 v153, v148, 5, s11
	s_waitcnt lgkmcnt(1)
	v_add_f32_e32 v148, v149, v151
	s_waitcnt lgkmcnt(0)
	v_max_f32_e32 v149, v152, v152
	v_max_f32_e32 v150, v150, v150
	v_max_f32_e32 v149, v150, v149
	ds_write_b64 v153, v[148:149]
.LBB0_748:
	s_or_b64 exec, exec, s[0:1]
	s_waitcnt lgkmcnt(0)
	v_or_b32_e32 v152, 32, v179
	v_add_u32_e32 v150, s10, v152
	v_mov_b32_e32 v151, 0
	v_lshlrev_b64 v[148:149], 11, v[150:151]
	v_readlane_b32 s60, v251, 11
	v_lshl_add_u64 v[158:159], v[148:149], 0, v[162:163]
	v_readlane_b32 s61, v251, 12
	s_brev_b32 s0, 60
	v_readlane_b32 s62, v251, 13
	v_lshl_add_u64 v[160:161], v[158:159], 2, s[60:61]
	v_lshl_add_u64 v[158:159], v[158:159], 1, s[22:23]
	v_readlane_b32 s63, v251, 14
	v_readlane_b32 s64, v251, 15
	v_readlane_b32 s65, v251, 16
	v_readlane_b32 s66, v251, 17
	v_readlane_b32 s67, v251, 18
	v_readlane_b32 s68, v251, 19
	v_readlane_b32 s69, v251, 20
	v_readlane_b32 s70, v251, 21
	v_readlane_b32 s71, v251, 22
	v_readlane_b32 s72, v251, 23
	v_readlane_b32 s73, v251, 24
	v_readlane_b32 s74, v251, 25
	v_readlane_b32 s75, v251, 26
	s_waitcnt vmcnt(12)
	v_mov_b32_e32 v154, v218
	v_mov_b32_e32 v155, v219
	v_mov_b32_e32 v156, v220
	v_mov_b32_e32 v157, v221
	v_pk_fma_f32 v[136:137], v[136:137], s[0:1], v[156:157] op_sel_hi:[1,0,1]
	v_pk_fma_f32 v[134:135], v[134:135], s[0:1], v[154:155] op_sel_hi:[1,0,1]
	v_cvt_pk_bf16_f32 v155, v136, v137
	v_cvt_pk_bf16_f32 v154, v134, v135
	global_store_dwordx2 v[158:159], v[154:155], off
	v_mul_f32_e32 v150, v135, v135
	v_mul_f32_e32 v153, v137, v137
	v_pk_mul_f32 v[166:167], v[14:15], v[134:135]
	v_fmac_f32_e32 v150, v134, v134
	v_fmac_f32_e32 v153, v136, v136
	v_add_f32_e32 v150, v150, v153
	s_waitcnt vmcnt(12)
	v_mov_b32_e32 v154, v222
	v_mov_b32_e32 v155, v223
	v_mov_b32_e32 v156, v224
	v_mov_b32_e32 v157, v225
	v_pk_fma_f32 v[140:141], v[140:141], s[0:1], v[156:157] op_sel_hi:[1,0,1]
	v_pk_fma_f32 v[138:139], v[138:139], s[0:1], v[154:155] op_sel_hi:[1,0,1]
	v_cvt_pk_bf16_f32 v155, v140, v141
	v_cvt_pk_bf16_f32 v154, v138, v139
	global_store_dwordx2 v[158:159], v[154:155], off offset:8
	v_mul_f32_e32 v169, v139, v139
	v_mul_f32_e32 v170, v141, v141
	v_fmac_f32_e32 v169, v138, v138
	v_fmac_f32_e32 v170, v140, v140
	s_waitcnt vmcnt(12)
	v_mov_b32_e32 v154, v226
	v_mov_b32_e32 v155, v227
	v_mov_b32_e32 v156, v228
	v_mov_b32_e32 v157, v229
	v_pk_fma_f32 v[128:129], v[128:129], s[0:1], v[156:157] op_sel_hi:[1,0,1]
	v_pk_fma_f32 v[126:127], v[126:127], s[0:1], v[154:155] op_sel_hi:[1,0,1]
	v_cvt_pk_bf16_f32 v155, v128, v129
	v_cvt_pk_bf16_f32 v154, v126, v127
	global_store_dwordx2 v[158:159], v[154:155], off offset:256
	v_pk_mul_f32 v[160:161], v[16:17], v[136:137]
	s_waitcnt vmcnt(12)
	v_mov_b32_e32 v154, v230
	v_mov_b32_e32 v155, v231
	v_mov_b32_e32 v156, v232
	v_mov_b32_e32 v157, v233
	s_mov_b32 s98, 0x100000
	s_mov_b32 s99, 0
	v_lshl_add_u64 v[230:231], v[198:199], 0, s[98:99]
	global_load_dwordx4 v[218:221], v[230:231], off
	global_load_dwordx4 v[222:225], v[230:231], off offset:16
	global_load_dwordx4 v[226:229], v[230:231], off offset:512
	global_load_dwordx4 v[230:233], v[230:231], off offset:528
	v_pk_fma_f32 v[144:145], v[144:145], s[0:1], v[156:157] op_sel_hi:[1,0,1]
	v_max_f32_e64 v160, |v160|, |v161|
	v_max3_f32 v153, |v166|, |v167|, v160
	v_pk_mul_f32 v[160:161], v[12:13], v[140:141]
	v_pk_mul_f32 v[166:167], v[10:11], v[138:139]
	v_max_f32_e64 v160, |v160|, |v161|
	v_add_f32_e32 v161, v169, v170
	v_max3_f32 v160, |v166|, |v167|, v160
	v_mul_f32_e32 v169, v127, v127
	v_mul_f32_e32 v170, v129, v129
	v_add_f32_e32 v150, v150, v161
	v_max3_f32 v153, v153, 0, v160
	v_pk_mul_f32 v[160:161], v[8:9], v[128:129]
	v_fmac_f32_e32 v169, v126, v126
	v_fmac_f32_e32 v170, v128, v128
	v_pk_mul_f32 v[166:167], v[6:7], v[126:127]
	v_max_f32_e64 v160, |v160|, |v161|
	v_add_f32_e32 v161, v169, v170
	v_pk_fma_f32 v[142:143], v[142:143], s[0:1], v[154:155] op_sel_hi:[1,0,1]
	v_pk_mul_f32 v[154:155], v[4:5], v[144:145]
	v_max3_f32 v160, |v166|, |v167|, v160
	v_add_f32_e32 v150, v150, v161
	v_mul_f32_e32 v161, v143, v143
	v_mul_f32_e32 v166, v145, v145
	v_pk_mul_f32 v[156:157], v[2:3], v[142:143]
	v_max_f32_e64 v154, |v154|, |v155|
	v_fmac_f32_e32 v161, v142, v142
	v_fmac_f32_e32 v166, v144, v144
	v_max3_f32 v154, |v156|, |v157|, v154
	v_add_f32_e32 v155, v161, v166
	v_max3_f32 v153, v153, v160, v154
	v_add_f32_e32 v150, v150, v155
	ds_bpermute_b32 v155, v168, v153
	ds_bpermute_b32 v154, v168, v150
	v_cvt_pk_bf16_f32 v156, v142, v143
	v_cvt_pk_bf16_f32 v157, v144, v145
	global_store_dwordx2 v[158:159], v[156:157], off offset:264
	s_waitcnt lgkmcnt(1)
	v_max_f32_e32 v155, v155, v155
	s_waitcnt lgkmcnt(0)
	v_add_f32_e32 v150, v150, v154
	v_max_f32_e32 v153, v153, v155
	ds_bpermute_b32 v154, v174, v150
	ds_bpermute_b32 v155, v174, v153
	s_and_saveexec_b64 s[14:15], s[2:3]
	s_cbranch_execz .LBB0_750
	v_lshl_add_u32 v156, v152, 5, s11
	s_waitcnt lgkmcnt(1)
	v_add_f32_e32 v152, v150, v154
	s_waitcnt lgkmcnt(0)
	v_max_f32_e32 v150, v155, v155
	v_max_f32_e32 v153, v153, v153
	v_max_f32_e32 v153, v153, v150
	ds_write_b64 v156, v[152:153]
.LBB0_750:
	s_or_b64 exec, exec, s[14:15]
	v_or_b32_e32 v152, 48, v179
	v_add_u32_e32 v150, s10, v152
	v_lshlrev_b64 v[150:151], 11, v[150:151]
	v_readlane_b32 s60, v251, 11
	v_lshl_add_u64 v[158:159], v[150:151], 0, v[162:163]
	v_readlane_b32 s61, v251, 12
	v_readlane_b32 s62, v251, 13
	v_readlane_b32 s63, v251, 14
	v_lshl_add_u64 v[160:161], v[158:159], 2, s[60:61]
	s_waitcnt lgkmcnt(0)
	v_lshl_add_u64 v[158:159], v[158:159], 1, s[22:23]
	v_readlane_b32 s64, v251, 15
	v_readlane_b32 s65, v251, 16
	v_readlane_b32 s66, v251, 17
	v_readlane_b32 s67, v251, 18
	v_readlane_b32 s68, v251, 19
	v_readlane_b32 s69, v251, 20
	v_readlane_b32 s70, v251, 21
	v_readlane_b32 s71, v251, 22
	v_readlane_b32 s72, v251, 23
	v_readlane_b32 s73, v251, 24
	v_readlane_b32 s74, v251, 25
	v_readlane_b32 s75, v251, 26
	s_waitcnt vmcnt(12)
	v_mov_b32_e32 v154, v234
	v_mov_b32_e32 v155, v235
	v_mov_b32_e32 v156, v236
	v_mov_b32_e32 v157, v237
	v_pk_fma_f32 v[132:133], v[132:133], s[0:1], v[156:157] op_sel_hi:[1,0,1]
	v_pk_fma_f32 v[130:131], v[130:131], s[0:1], v[154:155] op_sel_hi:[1,0,1]
	v_cvt_pk_bf16_f32 v155, v132, v133
	v_cvt_pk_bf16_f32 v154, v130, v131
	global_store_dwordx2 v[158:159], v[154:155], off
	v_mul_f32_e32 v153, v131, v131
	v_mul_f32_e32 v169, v133, v133
	v_pk_mul_f32 v[166:167], v[14:15], v[130:131]
	v_fmac_f32_e32 v153, v130, v130
	v_fmac_f32_e32 v169, v132, v132
	v_add_f32_e32 v153, v153, v169
	s_waitcnt vmcnt(12)
	v_mov_b32_e32 v154, v238
	v_mov_b32_e32 v155, v239
	v_mov_b32_e32 v156, v240
	v_mov_b32_e32 v157, v241
	v_pk_fma_f32 v[124:125], v[124:125], s[0:1], v[156:157] op_sel_hi:[1,0,1]
	v_pk_fma_f32 v[122:123], v[122:123], s[0:1], v[154:155] op_sel_hi:[1,0,1]
	v_cvt_pk_bf16_f32 v155, v124, v125
	v_cvt_pk_bf16_f32 v154, v122, v123
	global_store_dwordx2 v[158:159], v[154:155], off offset:8
	v_mul_f32_e32 v170, v123, v123
	v_mul_f32_e32 v171, v125, v125
	v_fmac_f32_e32 v170, v122, v122
	v_fmac_f32_e32 v171, v124, v124
	s_waitcnt vmcnt(12)
	v_mov_b32_e32 v154, v242
	v_mov_b32_e32 v155, v243
	v_mov_b32_e32 v156, v244
	v_mov_b32_e32 v157, v245
	v_pk_fma_f32 v[116:117], v[116:117], s[0:1], v[156:157] op_sel_hi:[1,0,1]
	v_pk_fma_f32 v[114:115], v[114:115], s[0:1], v[154:155] op_sel_hi:[1,0,1]
	v_cvt_pk_bf16_f32 v155, v116, v117
	v_cvt_pk_bf16_f32 v154, v114, v115
	global_store_dwordx2 v[158:159], v[154:155], off offset:256
	v_pk_mul_f32 v[160:161], v[16:17], v[132:133]
	s_waitcnt vmcnt(12)
	v_mov_b32_e32 v154, v246
	v_mov_b32_e32 v155, v247
	v_mov_b32_e32 v156, v248
	v_mov_b32_e32 v157, v249
	s_mov_b32 s98, 0x120000
	s_mov_b32 s99, 0
	v_lshl_add_u64 v[246:247], v[198:199], 0, s[98:99]
	global_load_dwordx4 v[234:237], v[246:247], off
	global_load_dwordx4 v[238:241], v[246:247], off offset:16
	global_load_dwordx4 v[242:245], v[246:247], off offset:512
	global_load_dwordx4 v[246:249], v[246:247], off offset:528
	v_pk_fma_f32 v[100:101], v[100:101], s[0:1], v[156:157] op_sel_hi:[1,0,1]
	v_max_f32_e64 v160, |v160|, |v161|
	v_max3_f32 v169, |v166|, |v167|, v160
	v_pk_mul_f32 v[160:161], v[12:13], v[124:125]
	v_pk_mul_f32 v[166:167], v[10:11], v[122:123]
	v_max_f32_e64 v160, |v160|, |v161|
	v_add_f32_e32 v161, v170, v171
	v_max3_f32 v160, |v166|, |v167|, v160
	v_mul_f32_e32 v170, v115, v115
	v_mul_f32_e32 v171, v117, v117
	v_add_f32_e32 v153, v153, v161
	v_max3_f32 v169, v169, 0, v160
	v_pk_mul_f32 v[160:161], v[8:9], v[116:117]
	v_fmac_f32_e32 v170, v114, v114
	v_fmac_f32_e32 v171, v116, v116
	v_pk_mul_f32 v[166:167], v[6:7], v[114:115]
	v_max_f32_e64 v160, |v160|, |v161|
	v_add_f32_e32 v161, v170, v171
	v_pk_fma_f32 v[98:99], v[98:99], s[0:1], v[154:155] op_sel_hi:[1,0,1]
	v_pk_mul_f32 v[154:155], v[4:5], v[100:101]
	v_max3_f32 v160, |v166|, |v167|, v160
	v_add_f32_e32 v153, v153, v161
	v_mul_f32_e32 v161, v99, v99
	v_mul_f32_e32 v166, v101, v101
	v_pk_mul_f32 v[156:157], v[2:3], v[98:99]
	v_max_f32_e64 v154, |v154|, |v155|
	v_fmac_f32_e32 v161, v98, v98
	v_fmac_f32_e32 v166, v100, v100
	v_max3_f32 v154, |v156|, |v157|, v154
	v_add_f32_e32 v155, v161, v166
	v_max3_f32 v154, v169, v160, v154
	v_add_f32_e32 v153, v153, v155
	ds_bpermute_b32 v156, v168, v154
	ds_bpermute_b32 v155, v168, v153
	v_cvt_pk_bf16_f32 v160, v98, v99
	v_cvt_pk_bf16_f32 v161, v100, v101
	global_store_dwordx2 v[158:159], v[160:161], off offset:264
	s_waitcnt lgkmcnt(1)
	v_max_f32_e32 v156, v156, v156
	s_waitcnt lgkmcnt(0)
	v_add_f32_e32 v153, v153, v155
	v_max_f32_e32 v154, v154, v156
	ds_bpermute_b32 v155, v174, v153
	ds_bpermute_b32 v156, v174, v154
	s_and_saveexec_b64 s[0:1], s[2:3]
	s_cbranch_execz .LBB0_752
	v_lshl_add_u32 v157, v152, 5, s11
	s_waitcnt lgkmcnt(1)
	v_add_f32_e32 v152, v153, v155
	s_waitcnt lgkmcnt(0)
	v_max_f32_e32 v153, v156, v156
	v_max_f32_e32 v154, v154, v154
	v_max_f32_e32 v153, v154, v153
	ds_write_b64 v157, v[152:153]
.LBB0_752:
	s_or_b64 exec, exec, s[0:1]
	s_waitcnt lgkmcnt(0)
	v_add_u32_e32 v156, 0x80, v179
	v_add_u32_e32 v154, s10, v156
	v_mov_b32_e32 v155, 0
	v_lshlrev_b64 v[152:153], 11, v[154:155]
	v_readlane_b32 s60, v251, 11
	v_lshl_add_u64 v[166:167], v[152:153], 0, v[162:163]
	v_readlane_b32 s61, v251, 12
	s_brev_b32 s0, 60
	v_readlane_b32 s62, v251, 13
	v_lshl_add_u64 v[170:171], v[166:167], 2, s[60:61]
	v_lshl_add_u64 v[166:167], v[166:167], 1, s[22:23]
	v_readlane_b32 s63, v251, 14
	v_readlane_b32 s64, v251, 15
	v_readlane_b32 s65, v251, 16
	v_readlane_b32 s66, v251, 17
	v_readlane_b32 s67, v251, 18
	v_readlane_b32 s68, v251, 19
	v_readlane_b32 s69, v251, 20
	v_readlane_b32 s70, v251, 21
	v_readlane_b32 s71, v251, 22
	v_readlane_b32 s72, v251, 23
	v_readlane_b32 s73, v251, 24
	v_readlane_b32 s74, v251, 25
	v_readlane_b32 s75, v251, 26
	s_waitcnt vmcnt(12)
	v_mov_b32_e32 v158, v218
	v_mov_b32_e32 v159, v219
	v_mov_b32_e32 v160, v220
	v_mov_b32_e32 v161, v221
	v_pk_fma_f32 v[96:97], v[96:97], s[0:1], v[160:161] op_sel_hi:[1,0,1]
	v_pk_fma_f32 v[94:95], v[94:95], s[0:1], v[158:159] op_sel_hi:[1,0,1]
	v_cvt_pk_bf16_f32 v159, v96, v97
	v_cvt_pk_bf16_f32 v158, v94, v95
	global_store_dwordx2 v[166:167], v[158:159], off
	v_mul_f32_e32 v154, v95, v95
	v_mul_f32_e32 v157, v97, v97
	v_pk_mul_f32 v[172:173], v[14:15], v[94:95]
	v_fmac_f32_e32 v154, v94, v94
	v_fmac_f32_e32 v157, v96, v96
	v_add_f32_e32 v154, v154, v157
	s_waitcnt vmcnt(12)
	v_mov_b32_e32 v158, v222
	v_mov_b32_e32 v159, v223
	v_mov_b32_e32 v160, v224
	v_mov_b32_e32 v161, v225
	v_pk_fma_f32 v[92:93], v[92:93], s[0:1], v[160:161] op_sel_hi:[1,0,1]
	v_pk_fma_f32 v[90:91], v[90:91], s[0:1], v[158:159] op_sel_hi:[1,0,1]
	v_cvt_pk_bf16_f32 v159, v92, v93
	v_cvt_pk_bf16_f32 v158, v90, v91
	global_store_dwordx2 v[166:167], v[158:159], off offset:8
	v_mul_f32_e32 v175, v93, v93
	v_fmac_f32_e32 v175, v92, v92
	s_waitcnt vmcnt(12)
	v_mov_b32_e32 v158, v226
	v_mov_b32_e32 v159, v227
	v_mov_b32_e32 v160, v228
	v_mov_b32_e32 v161, v229
	v_pk_fma_f32 v[88:89], v[88:89], s[0:1], v[160:161] op_sel_hi:[1,0,1]
	v_pk_fma_f32 v[86:87], v[86:87], s[0:1], v[158:159] op_sel_hi:[1,0,1]
	v_cvt_pk_bf16_f32 v159, v88, v89
	v_cvt_pk_bf16_f32 v158, v86, v87
	global_store_dwordx2 v[166:167], v[158:159], off offset:256
	v_pk_mul_f32 v[170:171], v[16:17], v[96:97]
	s_waitcnt vmcnt(12)
	v_mov_b32_e32 v158, v230
	v_mov_b32_e32 v159, v231
	v_mov_b32_e32 v160, v232
	v_mov_b32_e32 v161, v233
	s_mov_b32 s98, 0x140000
	s_mov_b32 s99, 0
	v_lshl_add_u64 v[230:231], v[198:199], 0, s[98:99]
	global_load_dwordx4 v[218:221], v[230:231], off
	global_load_dwordx4 v[222:225], v[230:231], off offset:16
	global_load_dwordx4 v[226:229], v[230:231], off offset:512
	global_load_dwordx4 v[230:233], v[230:231], off offset:528
	v_pk_fma_f32 v[84:85], v[84:85], s[0:1], v[160:161] op_sel_hi:[1,0,1]
	v_max_f32_e64 v169, |v170|, |v171|
	v_max3_f32 v157, |v172|, |v173|, v169
	v_mul_f32_e32 v169, v91, v91
	v_fmac_f32_e32 v169, v90, v90
	v_pk_mul_f32 v[170:171], v[12:13], v[92:93]
	v_add_f32_e32 v169, v169, v175
	v_pk_mul_f32 v[172:173], v[10:11], v[90:91]
	v_max_f32_e64 v170, |v170|, |v171|
	v_add_f32_e32 v154, v154, v169
	v_mul_f32_e32 v169, v87, v87
	v_mul_f32_e32 v175, v89, v89
	v_max3_f32 v170, |v172|, |v173|, v170
	v_fmac_f32_e32 v169, v86, v86
	v_fmac_f32_e32 v175, v88, v88
	v_max3_f32 v157, v157, 0, v170
	v_pk_mul_f32 v[170:171], v[8:9], v[88:89]
	v_add_f32_e32 v169, v169, v175
	v_pk_fma_f32 v[82:83], v[82:83], s[0:1], v[158:159] op_sel_hi:[1,0,1]
	v_pk_mul_f32 v[158:159], v[4:5], v[84:85]
	v_pk_mul_f32 v[172:173], v[6:7], v[86:87]
	v_max_f32_e64 v170, |v170|, |v171|
	v_add_f32_e32 v154, v154, v169
	v_mul_f32_e32 v169, v83, v83
	v_mul_f32_e32 v171, v85, v85
	v_pk_mul_f32 v[160:161], v[2:3], v[82:83]
	v_max_f32_e64 v158, |v158|, |v159|
	v_max3_f32 v170, |v172|, |v173|, v170
	v_fmac_f32_e32 v169, v82, v82
	v_fmac_f32_e32 v171, v84, v84
	v_max3_f32 v158, |v160|, |v161|, v158
	v_add_f32_e32 v159, v169, v171
	v_max3_f32 v157, v157, v170, v158
	v_add_f32_e32 v154, v154, v159
	ds_bpermute_b32 v159, v168, v157
	ds_bpermute_b32 v158, v168, v154
	v_cvt_pk_bf16_f32 v160, v82, v83
	v_cvt_pk_bf16_f32 v161, v84, v85
	global_store_dwordx2 v[166:167], v[160:161], off offset:264
	s_waitcnt lgkmcnt(1)
	v_max_f32_e32 v159, v159, v159
	s_waitcnt lgkmcnt(0)
	v_add_f32_e32 v154, v154, v158
	v_max_f32_e32 v157, v157, v159
	ds_bpermute_b32 v158, v174, v154
	ds_bpermute_b32 v159, v174, v157
	s_and_saveexec_b64 s[14:15], s[2:3]
	s_cbranch_execz .LBB0_754
	v_lshl_add_u32 v160, v156, 5, s11
	s_waitcnt lgkmcnt(1)
	v_add_f32_e32 v156, v154, v158
	s_waitcnt lgkmcnt(0)
	v_max_f32_e32 v154, v159, v159
	v_max_f32_e32 v157, v157, v157
	v_max_f32_e32 v157, v157, v154
	ds_write_b64 v160, v[156:157]
.LBB0_754:
	s_or_b64 exec, exec, s[14:15]
	v_add_u32_e32 v156, 0x90, v179
	v_add_u32_e32 v154, s10, v156
	v_lshlrev_b64 v[154:155], 11, v[154:155]
	v_readlane_b32 s60, v251, 11
	v_lshl_add_u64 v[166:167], v[154:155], 0, v[162:163]
	v_readlane_b32 s61, v251, 12
	v_readlane_b32 s62, v251, 13
	v_readlane_b32 s63, v251, 14
	v_lshl_add_u64 v[170:171], v[166:167], 2, s[60:61]
	s_waitcnt lgkmcnt(0)
	v_lshl_add_u64 v[166:167], v[166:167], 1, s[22:23]
	v_readlane_b32 s64, v251, 15
	v_readlane_b32 s65, v251, 16
	v_readlane_b32 s66, v251, 17
	v_readlane_b32 s67, v251, 18
	v_readlane_b32 s68, v251, 19
	v_readlane_b32 s69, v251, 20
	v_readlane_b32 s70, v251, 21
	v_readlane_b32 s71, v251, 22
	v_readlane_b32 s72, v251, 23
	v_readlane_b32 s73, v251, 24
	v_readlane_b32 s74, v251, 25
	v_readlane_b32 s75, v251, 26
	s_waitcnt vmcnt(12)
	v_mov_b32_e32 v158, v234
	v_mov_b32_e32 v159, v235
	v_mov_b32_e32 v160, v236
	v_mov_b32_e32 v161, v237
	v_pk_fma_f32 v[80:81], v[80:81], s[0:1], v[160:161] op_sel_hi:[1,0,1]
	v_pk_fma_f32 v[78:79], v[78:79], s[0:1], v[158:159] op_sel_hi:[1,0,1]
	v_cvt_pk_bf16_f32 v159, v80, v81
	v_cvt_pk_bf16_f32 v158, v78, v79
	global_store_dwordx2 v[166:167], v[158:159], off
	v_mul_f32_e32 v157, v79, v79
	v_mul_f32_e32 v169, v81, v81
	v_pk_mul_f32 v[172:173], v[14:15], v[78:79]
	v_fmac_f32_e32 v157, v78, v78
	v_fmac_f32_e32 v169, v80, v80
	v_add_f32_e32 v157, v157, v169
	s_waitcnt vmcnt(12)
	v_mov_b32_e32 v158, v238
	v_mov_b32_e32 v159, v239
	v_mov_b32_e32 v160, v240
	v_mov_b32_e32 v161, v241
	v_pk_fma_f32 v[76:77], v[76:77], s[0:1], v[160:161] op_sel_hi:[1,0,1]
	v_pk_fma_f32 v[74:75], v[74:75], s[0:1], v[158:159] op_sel_hi:[1,0,1]
	v_cvt_pk_bf16_f32 v159, v76, v77
	v_cvt_pk_bf16_f32 v158, v74, v75
	global_store_dwordx2 v[166:167], v[158:159], off offset:8
	v_mul_f32_e32 v175, v75, v75
	v_mul_f32_e32 v176, v77, v77
	v_fmac_f32_e32 v175, v74, v74
	v_fmac_f32_e32 v176, v76, v76
	s_waitcnt vmcnt(12)
	v_mov_b32_e32 v158, v242
	v_mov_b32_e32 v159, v243
	v_mov_b32_e32 v160, v244
	v_mov_b32_e32 v161, v245
	v_pk_fma_f32 v[72:73], v[72:73], s[0:1], v[160:161] op_sel_hi:[1,0,1]
	v_pk_fma_f32 v[70:71], v[70:71], s[0:1], v[158:159] op_sel_hi:[1,0,1]
	v_cvt_pk_bf16_f32 v159, v72, v73
	v_cvt_pk_bf16_f32 v158, v70, v71
	global_store_dwordx2 v[166:167], v[158:159], off offset:256
	v_pk_mul_f32 v[170:171], v[16:17], v[80:81]
	s_waitcnt vmcnt(12)
	v_mov_b32_e32 v158, v246
	v_mov_b32_e32 v159, v247
	v_mov_b32_e32 v160, v248
	v_mov_b32_e32 v161, v249
	s_mov_b32 s98, 0x160000
	s_mov_b32 s99, 0
	v_lshl_add_u64 v[246:247], v[198:199], 0, s[98:99]
	global_load_dwordx4 v[234:237], v[246:247], off
	global_load_dwordx4 v[238:241], v[246:247], off offset:16
	global_load_dwordx4 v[242:245], v[246:247], off offset:512
	global_load_dwordx4 v[246:249], v[246:247], off offset:528
	v_pk_fma_f32 v[68:69], v[68:69], s[0:1], v[160:161] op_sel_hi:[1,0,1]
	v_max_f32_e64 v170, |v170|, |v171|
	v_max3_f32 v169, |v172|, |v173|, v170
	v_pk_mul_f32 v[170:171], v[12:13], v[76:77]
	v_pk_mul_f32 v[172:173], v[10:11], v[74:75]
	v_max_f32_e64 v170, |v170|, |v171|
	v_add_f32_e32 v171, v175, v176
	v_max3_f32 v170, |v172|, |v173|, v170
	v_mul_f32_e32 v175, v71, v71
	v_mul_f32_e32 v176, v73, v73
	v_add_f32_e32 v157, v157, v171
	v_max3_f32 v169, v169, 0, v170
	v_pk_mul_f32 v[170:171], v[8:9], v[72:73]
	v_fmac_f32_e32 v175, v70, v70
	v_fmac_f32_e32 v176, v72, v72
	v_pk_mul_f32 v[172:173], v[6:7], v[70:71]
	v_max_f32_e64 v170, |v170|, |v171|
	v_add_f32_e32 v171, v175, v176
	v_pk_fma_f32 v[66:67], v[66:67], s[0:1], v[158:159] op_sel_hi:[1,0,1]
	v_pk_mul_f32 v[158:159], v[4:5], v[68:69]
	v_max3_f32 v170, |v172|, |v173|, v170
	v_add_f32_e32 v157, v157, v171
	v_mul_f32_e32 v171, v67, v67
	v_mul_f32_e32 v172, v69, v69
	v_pk_mul_f32 v[160:161], v[2:3], v[66:67]
	v_max_f32_e64 v158, |v158|, |v159|
	v_fmac_f32_e32 v171, v66, v66
	v_fmac_f32_e32 v172, v68, v68
	v_max3_f32 v158, |v160|, |v161|, v158
	v_add_f32_e32 v159, v171, v172
	v_max3_f32 v158, v169, v170, v158
	v_add_f32_e32 v157, v157, v159
	ds_bpermute_b32 v160, v168, v158
	ds_bpermute_b32 v159, v168, v157
	v_cvt_pk_bf16_f32 v170, v66, v67
	v_cvt_pk_bf16_f32 v171, v68, v69
	global_store_dwordx2 v[166:167], v[170:171], off offset:264
	s_waitcnt lgkmcnt(1)
	v_max_f32_e32 v160, v160, v160
	s_waitcnt lgkmcnt(0)
	v_add_f32_e32 v157, v157, v159
	v_max_f32_e32 v158, v158, v160
	ds_bpermute_b32 v159, v174, v157
	ds_bpermute_b32 v160, v174, v158
	s_and_saveexec_b64 s[0:1], s[2:3]
	s_cbranch_execz .LBB0_756
	v_lshl_add_u32 v161, v156, 5, s11
	s_waitcnt lgkmcnt(1)
	v_add_f32_e32 v156, v157, v159
	s_waitcnt lgkmcnt(0)
	v_max_f32_e32 v157, v160, v160
	v_max_f32_e32 v158, v158, v158
	v_max_f32_e32 v157, v158, v157
	ds_write_b64 v161, v[156:157]
.LBB0_756:
	s_or_b64 exec, exec, s[0:1]
	s_waitcnt lgkmcnt(0)
	v_add_u32_e32 v160, 0xa0, v179
	v_add_u32_e32 v158, s10, v160
	v_mov_b32_e32 v159, 0
	v_lshlrev_b64 v[156:157], 11, v[158:159]
	v_readlane_b32 s60, v251, 11
	v_lshl_add_u64 v[166:167], v[156:157], 0, v[162:163]
	v_readlane_b32 s61, v251, 12
	s_brev_b32 s0, 60
	v_lshl_add_u64 v[180:181], v[166:167], 1, s[22:23]
	v_lshl_add_u64 v[176:177], v[166:167], 2, s[60:61]
	v_readlane_b32 s62, v251, 13
	v_readlane_b32 s63, v251, 14
	v_readlane_b32 s64, v251, 15
	v_readlane_b32 s65, v251, 16
	v_readlane_b32 s66, v251, 17
	v_readlane_b32 s67, v251, 18
	v_readlane_b32 s68, v251, 19
	v_readlane_b32 s69, v251, 20
	v_readlane_b32 s70, v251, 21
	v_readlane_b32 s71, v251, 22
	v_readlane_b32 s72, v251, 23
	v_readlane_b32 s73, v251, 24
	v_readlane_b32 s74, v251, 25
	v_readlane_b32 s75, v251, 26
	s_waitcnt vmcnt(12)
	v_mov_b32_e32 v170, v218
	v_mov_b32_e32 v171, v219
	v_mov_b32_e32 v172, v220
	v_mov_b32_e32 v173, v221
	v_pk_fma_f32 v[64:65], v[64:65], s[0:1], v[172:173] op_sel_hi:[1,0,1]
	v_pk_fma_f32 v[62:63], v[62:63], s[0:1], v[170:171] op_sel_hi:[1,0,1]
	v_cvt_pk_bf16_f32 v167, v64, v65
	v_cvt_pk_bf16_f32 v166, v62, v63
	global_store_dwordx2 v[180:181], v[166:167], off
	v_mul_f32_e32 v158, v63, v63
	v_mul_f32_e32 v161, v65, v65
	v_fmac_f32_e32 v158, v62, v62
	v_fmac_f32_e32 v161, v64, v64
	v_add_f32_e32 v158, v158, v161
	s_waitcnt vmcnt(12)
	v_mov_b32_e32 v170, v222
	v_mov_b32_e32 v171, v223
	v_mov_b32_e32 v172, v224
	v_mov_b32_e32 v173, v225
	v_pk_fma_f32 v[60:61], v[60:61], s[0:1], v[172:173] op_sel_hi:[1,0,1]
	v_pk_fma_f32 v[58:59], v[58:59], s[0:1], v[170:171] op_sel_hi:[1,0,1]
	v_cvt_pk_bf16_f32 v167, v60, v61
	v_cvt_pk_bf16_f32 v166, v58, v59
	global_store_dwordx2 v[180:181], v[166:167], off offset:8
	v_mul_f32_e32 v169, v59, v59
	v_mul_f32_e32 v175, v61, v61
	v_fmac_f32_e32 v169, v58, v58
	v_fmac_f32_e32 v175, v60, v60
	s_waitcnt vmcnt(12)
	v_mov_b32_e32 v170, v226
	v_mov_b32_e32 v171, v227
	v_mov_b32_e32 v172, v228
	v_mov_b32_e32 v173, v229
	v_pk_fma_f32 v[56:57], v[56:57], s[0:1], v[172:173] op_sel_hi:[1,0,1]
	v_pk_fma_f32 v[54:55], v[54:55], s[0:1], v[170:171] op_sel_hi:[1,0,1]
	v_cvt_pk_bf16_f32 v167, v56, v57
	v_cvt_pk_bf16_f32 v166, v54, v55
	global_store_dwordx2 v[180:181], v[166:167], off offset:256
	v_pk_mul_f32 v[166:167], v[16:17], v[64:65]
	v_pk_mul_f32 v[176:177], v[14:15], v[62:63]
	v_max_f32_e64 v166, |v166|, |v167|
	v_max3_f32 v161, |v176|, |v177|, v166
	v_pk_mul_f32 v[166:167], v[12:13], v[60:61]
	v_pk_mul_f32 v[176:177], v[10:11], v[58:59]
	v_max_f32_e64 v166, |v166|, |v167|
	v_add_f32_e32 v167, v169, v175
	v_max3_f32 v166, |v176|, |v177|, v166
	v_mul_f32_e32 v169, v55, v55
	v_mul_f32_e32 v175, v57, v57
	v_add_f32_e32 v158, v158, v167
	v_max3_f32 v161, v161, 0, v166
	v_pk_mul_f32 v[166:167], v[8:9], v[56:57]
	v_fmac_f32_e32 v169, v54, v54
	v_fmac_f32_e32 v175, v56, v56
	v_pk_mul_f32 v[176:177], v[6:7], v[54:55]
	v_max_f32_e64 v166, |v166|, |v167|
	v_add_f32_e32 v167, v169, v175
	v_max3_f32 v169, |v176|, |v177|, v166
	v_add_f32_e32 v158, v158, v167
	s_waitcnt vmcnt(12)
	v_mov_b32_e32 v170, v230
	v_mov_b32_e32 v171, v231
	v_mov_b32_e32 v172, v232
	v_mov_b32_e32 v173, v233
	v_pk_fma_f32 v[52:53], v[52:53], s[0:1], v[172:173] op_sel_hi:[1,0,1]
	v_pk_fma_f32 v[50:51], v[50:51], s[0:1], v[170:171] op_sel_hi:[1,0,1]
	v_pk_mul_f32 v[166:167], v[4:5], v[52:53]
	v_mul_f32_e32 v172, v51, v51
	v_mul_f32_e32 v173, v53, v53
	v_pk_mul_f32 v[170:171], v[2:3], v[50:51]
	v_max_f32_e64 v166, |v166|, |v167|
	v_fmac_f32_e32 v172, v50, v50
	v_fmac_f32_e32 v173, v52, v52
	v_max3_f32 v166, |v170|, |v171|, v166
	v_add_f32_e32 v167, v172, v173
	v_max3_f32 v161, v161, v169, v166
	v_add_f32_e32 v158, v158, v167
	ds_bpermute_b32 v167, v168, v161
	ds_bpermute_b32 v166, v168, v158
	v_cvt_pk_bf16_f32 v170, v50, v51
	v_cvt_pk_bf16_f32 v171, v52, v53
	global_store_dwordx2 v[180:181], v[170:171], off offset:264
	s_waitcnt lgkmcnt(1)
	v_max_f32_e32 v167, v167, v167
	s_waitcnt lgkmcnt(0)
	v_add_f32_e32 v158, v158, v166
	v_max_f32_e32 v161, v161, v167
	ds_bpermute_b32 v166, v174, v158
	ds_bpermute_b32 v167, v174, v161
	s_and_saveexec_b64 s[14:15], s[2:3]
	s_cbranch_execz .LBB0_758
	v_lshl_add_u32 v169, v160, 5, s11
	s_waitcnt lgkmcnt(1)
	v_add_f32_e32 v160, v158, v166
	s_waitcnt lgkmcnt(0)
	v_max_f32_e32 v158, v167, v167
	v_max_f32_e32 v161, v161, v161
	v_max_f32_e32 v161, v161, v158
	ds_write_b64 v169, v[160:161]
.LBB0_758:
	s_or_b64 exec, exec, s[14:15]
	v_add_u32_e32 v160, 0xb0, v179
	v_add_u32_e32 v158, s10, v160
	v_lshlrev_b64 v[158:159], 11, v[158:159]
	v_readlane_b32 s60, v251, 11
	s_waitcnt lgkmcnt(0)
	v_lshl_add_u64 v[166:167], v[158:159], 0, v[162:163]
	v_readlane_b32 s61, v251, 12
	v_lshl_add_u64 v[180:181], v[166:167], 1, s[22:23]
	v_readlane_b32 s62, v251, 13
	v_lshl_add_u64 v[176:177], v[166:167], 2, s[60:61]
	v_readlane_b32 s63, v251, 14
	v_readlane_b32 s64, v251, 15
	v_readlane_b32 s65, v251, 16
	v_readlane_b32 s66, v251, 17
	v_readlane_b32 s67, v251, 18
	v_readlane_b32 s68, v251, 19
	v_readlane_b32 s69, v251, 20
	v_readlane_b32 s70, v251, 21
	v_readlane_b32 s71, v251, 22
	v_readlane_b32 s72, v251, 23
	v_readlane_b32 s73, v251, 24
	v_readlane_b32 s74, v251, 25
	v_readlane_b32 s75, v251, 26
	s_waitcnt vmcnt(8)
	v_mov_b32_e32 v170, v234
	v_mov_b32_e32 v171, v235
	v_mov_b32_e32 v172, v236
	v_mov_b32_e32 v173, v237
	v_pk_fma_f32 v[48:49], v[48:49], s[0:1], v[172:173] op_sel_hi:[1,0,1]
	v_pk_fma_f32 v[46:47], v[46:47], s[0:1], v[170:171] op_sel_hi:[1,0,1]
	v_cvt_pk_bf16_f32 v167, v48, v49
	v_cvt_pk_bf16_f32 v166, v46, v47
	global_store_dwordx2 v[180:181], v[166:167], off
	v_mul_f32_e32 v161, v47, v47
	v_mul_f32_e32 v169, v49, v49
	v_fmac_f32_e32 v161, v46, v46
	v_fmac_f32_e32 v169, v48, v48
	v_add_f32_e32 v161, v161, v169
	s_waitcnt vmcnt(8)
	v_mov_b32_e32 v170, v238
	v_mov_b32_e32 v171, v239
	v_mov_b32_e32 v172, v240
	v_mov_b32_e32 v173, v241
	v_pk_fma_f32 v[44:45], v[44:45], s[0:1], v[172:173] op_sel_hi:[1,0,1]
	v_pk_fma_f32 v[42:43], v[42:43], s[0:1], v[170:171] op_sel_hi:[1,0,1]
	v_cvt_pk_bf16_f32 v167, v44, v45
	v_cvt_pk_bf16_f32 v166, v42, v43
	global_store_dwordx2 v[180:181], v[166:167], off offset:8
	v_mul_f32_e32 v175, v43, v43
	v_mul_f32_e32 v182, v45, v45
	v_fmac_f32_e32 v175, v42, v42
	v_fmac_f32_e32 v182, v44, v44
	s_waitcnt vmcnt(8)
	v_mov_b32_e32 v170, v242
	v_mov_b32_e32 v171, v243
	v_mov_b32_e32 v172, v244
	v_mov_b32_e32 v173, v245
	v_pk_fma_f32 v[40:41], v[40:41], s[0:1], v[172:173] op_sel_hi:[1,0,1]
	v_pk_fma_f32 v[38:39], v[38:39], s[0:1], v[170:171] op_sel_hi:[1,0,1]
	v_cvt_pk_bf16_f32 v167, v40, v41
	v_cvt_pk_bf16_f32 v166, v38, v39
	global_store_dwordx2 v[180:181], v[166:167], off offset:256
	v_pk_mul_f32 v[166:167], v[16:17], v[48:49]
	v_pk_mul_f32 v[176:177], v[14:15], v[46:47]
	v_max_f32_e64 v166, |v166|, |v167|
	v_max3_f32 v169, |v176|, |v177|, v166
	v_pk_mul_f32 v[166:167], v[12:13], v[44:45]
	v_pk_mul_f32 v[176:177], v[10:11], v[42:43]
	v_max_f32_e64 v166, |v166|, |v167|
	v_add_f32_e32 v167, v175, v182
	v_max3_f32 v166, |v176|, |v177|, v166
	v_mul_f32_e32 v175, v39, v39
	v_mul_f32_e32 v182, v41, v41
	v_add_f32_e32 v161, v161, v167
	v_max3_f32 v169, v169, 0, v166
	v_pk_mul_f32 v[166:167], v[8:9], v[40:41]
	v_fmac_f32_e32 v175, v38, v38
	v_fmac_f32_e32 v182, v40, v40
	v_pk_mul_f32 v[176:177], v[6:7], v[38:39]
	v_max_f32_e64 v166, |v166|, |v167|
	v_add_f32_e32 v167, v175, v182
	v_max3_f32 v175, |v176|, |v177|, v166
	v_add_f32_e32 v161, v161, v167
	s_waitcnt vmcnt(8)
	v_mov_b32_e32 v170, v246
	v_mov_b32_e32 v171, v247
	v_mov_b32_e32 v172, v248
	v_mov_b32_e32 v173, v249
	v_pk_fma_f32 v[36:37], v[36:37], s[0:1], v[172:173] op_sel_hi:[1,0,1]
	v_pk_fma_f32 v[34:35], v[34:35], s[0:1], v[170:171] op_sel_hi:[1,0,1]
	v_mul_f32_e32 v173, v37, v37
	v_mul_f32_e32 v172, v35, v35
	v_pk_mul_f32 v[166:167], v[4:5], v[36:37]
	v_pk_mul_f32 v[170:171], v[2:3], v[34:35]
	v_fmac_f32_e32 v172, v34, v34
	v_fmac_f32_e32 v173, v36, v36
	v_max_f32_e64 v166, |v166|, |v167|
	v_add_f32_e32 v167, v172, v173
	v_max3_f32 v166, |v170|, |v171|, v166
	v_add_f32_e32 v161, v161, v167
	v_max3_f32 v166, v169, v175, v166
	ds_bpermute_b32 v167, v168, v161
	ds_bpermute_b32 v168, v168, v166
	v_cvt_pk_bf16_f32 v170, v34, v35
	v_cvt_pk_bf16_f32 v171, v36, v37
	global_store_dwordx2 v[180:181], v[170:171], off offset:264
	s_waitcnt lgkmcnt(1)
	v_add_f32_e32 v161, v161, v167
	s_waitcnt lgkmcnt(0)
	v_max_f32_e32 v168, v168, v168
	v_max_f32_e32 v166, v166, v168
	ds_bpermute_b32 v167, v174, v161
	ds_bpermute_b32 v168, v174, v166
	s_and_saveexec_b64 s[0:1], s[2:3]
	s_cbranch_execz .LBB0_760
	v_lshl_add_u32 v169, v160, 5, s11
	s_waitcnt lgkmcnt(1)
	v_add_f32_e32 v160, v161, v167
	s_waitcnt lgkmcnt(0)
	v_max_f32_e32 v161, v168, v168
	v_max_f32_e32 v166, v166, v166
	v_max_f32_e32 v161, v166, v161
	ds_write_b64 v169, v[160:161]

.LBB0_1602:
	v_lshl_add_u32 v14, s74, 8, v168
	v_ashrrev_i32_e32 v15, 31, v14
	s_nop 15
	s_nop 7
	v_lshl_add_u64 v[2:3], v[14:15], 2, s[28:29]
	global_load_dword v8, v[2:3], off
	global_load_dword v233, v[2:3], off offset:64
	global_load_dword v234, v[2:3], off offset:128
	global_load_dword v235, v[2:3], off offset:192
	global_load_dword v236, v[2:3], off offset:512
	global_load_dword v237, v[2:3], off offset:576
	global_load_dword v238, v[2:3], off offset:640
	global_load_dword v239, v[2:3], off offset:704
	v_lshl_or_b32 v4, s75, 8, v170
	v_ashrrev_i32_e32 v5, 31, v4
	v_lshlrev_b64 v[6:7], 12, v[14:15]
	v_lshlrev_b64 v[18:19], 1, v[4:5]
	v_lshl_add_u64 v[4:5], s[26:27], 0, v[6:7]
	v_or_b32_e32 v16, 16, v14
	v_ashrrev_i32_e32 v17, 31, v16
	v_lshl_add_u64 v[4:5], v[4:5], 0, v[18:19]
	v_lshl_add_u64 v[20:21], v[16:17], 2, s[28:29]
	s_waitcnt vmcnt(0)
	v_mul_f32_e32 v6, 0x3c000000, v8
	v_pk_mul_f32 v[8:9], v[148:149], v[6:7] op_sel_hi:[1,0]
	v_pk_mul_f32 v[10:11], v[146:147], v[6:7] op_sel_hi:[1,0]
	v_pk_mul_f32 v[12:13], v[152:153], v[6:7] op_sel_hi:[1,0]
	v_pk_mul_f32 v[22:23], v[150:151], v[6:7] op_sel_hi:[1,0]
	v_pk_mul_f32 v[24:25], v[156:157], v[6:7] op_sel_hi:[1,0]
	v_pk_mul_f32 v[26:27], v[154:155], v[6:7] op_sel_hi:[1,0]
	v_pk_mul_f32 v[28:29], v[160:161], v[6:7] op_sel_hi:[1,0]
	v_pk_mul_f32 v[30:31], v[158:159], v[6:7] op_sel_hi:[1,0]
	v_cvt_pk_bf16_f32 v6, v10, v11
	v_cvt_pk_bf16_f32 v7, v8, v9
	v_cvt_pk_bf16_f32 v8, v22, v23
	v_cvt_pk_bf16_f32 v9, v12, v13
	v_cvt_pk_bf16_f32 v10, v26, v27
	v_cvt_pk_bf16_f32 v11, v24, v25
	v_cvt_pk_bf16_f32 v12, v30, v31
	v_cvt_pk_bf16_f32 v13, v28, v29
	global_store_dwordx4 v[4:5], v[6:9], off
	global_store_dwordx4 v[4:5], v[10:13], off offset:256
	v_lshlrev_b64 v[6:7], 12, v[16:17]
	v_lshl_add_u64 v[6:7], s[26:27], 0, v[6:7]
	v_lshl_add_u64 v[22:23], v[6:7], 0, v[18:19]
	v_or_b32_e32 v20, 32, v14
	v_ashrrev_i32_e32 v21, 31, v20
	v_lshl_add_u64 v[16:17], v[20:21], 2, s[28:29]
	v_or_b32_e32 v14, 48, v14
	v_ashrrev_i32_e32 v15, 31, v14
	v_mov_b32_e32 v8, v233
	v_mul_f32_e32 v6, 0x3c000000, v8
	v_pk_mul_f32 v[8:9], v[144:145], v[6:7] op_sel_hi:[1,0]
	v_pk_mul_f32 v[10:11], v[142:143], v[6:7] op_sel_hi:[1,0]
	v_pk_mul_f32 v[12:13], v[140:141], v[6:7] op_sel_hi:[1,0]
	v_pk_mul_f32 v[24:25], v[138:139], v[6:7] op_sel_hi:[1,0]
	v_pk_mul_f32 v[26:27], v[136:137], v[6:7] op_sel_hi:[1,0]
	v_pk_mul_f32 v[28:29], v[134:135], v[6:7] op_sel_hi:[1,0]
	v_pk_mul_f32 v[30:31], v[132:133], v[6:7] op_sel_hi:[1,0]
	v_pk_mul_f32 v[32:33], v[130:131], v[6:7] op_sel_hi:[1,0]
	v_cvt_pk_bf16_f32 v6, v10, v11
	v_cvt_pk_bf16_f32 v7, v8, v9
	v_cvt_pk_bf16_f32 v8, v24, v25
	v_cvt_pk_bf16_f32 v9, v12, v13
	v_cvt_pk_bf16_f32 v10, v28, v29
	v_cvt_pk_bf16_f32 v11, v26, v27
	v_cvt_pk_bf16_f32 v12, v32, v33
	v_cvt_pk_bf16_f32 v13, v30, v31
	global_store_dwordx4 v[22:23], v[6:9], off
	global_store_dwordx4 v[22:23], v[10:13], off offset:256
	v_lshlrev_b64 v[6:7], 12, v[20:21]
	v_lshl_add_u64 v[6:7], s[26:27], 0, v[6:7]
	v_lshl_add_u64 v[20:21], v[6:7], 0, v[18:19]
	v_lshl_add_u64 v[16:17], v[14:15], 2, s[28:29]
	v_mov_b32_e32 v8, v234
	v_mul_f32_e32 v6, 0x3c000000, v8
	v_pk_mul_f32 v[8:9], v[128:129], v[6:7] op_sel_hi:[1,0]
	v_pk_mul_f32 v[10:11], v[126:127], v[6:7] op_sel_hi:[1,0]
	v_pk_mul_f32 v[12:13], v[124:125], v[6:7] op_sel_hi:[1,0]
	v_pk_mul_f32 v[22:23], v[122:123], v[6:7] op_sel_hi:[1,0]
	v_pk_mul_f32 v[24:25], v[120:121], v[6:7] op_sel_hi:[1,0]
	v_pk_mul_f32 v[26:27], v[118:119], v[6:7] op_sel_hi:[1,0]
	v_pk_mul_f32 v[28:29], v[116:117], v[6:7] op_sel_hi:[1,0]
	v_pk_mul_f32 v[30:31], v[114:115], v[6:7] op_sel_hi:[1,0]
	v_cvt_pk_bf16_f32 v6, v10, v11
	v_cvt_pk_bf16_f32 v7, v8, v9
	v_cvt_pk_bf16_f32 v8, v22, v23
	v_cvt_pk_bf16_f32 v9, v12, v13
	v_cvt_pk_bf16_f32 v10, v26, v27
	v_cvt_pk_bf16_f32 v11, v24, v25
	v_cvt_pk_bf16_f32 v12, v30, v31
	v_cvt_pk_bf16_f32 v13, v28, v29
	global_store_dwordx4 v[20:21], v[6:9], off
	global_store_dwordx4 v[20:21], v[10:13], off offset:256
	v_lshlrev_b64 v[6:7], 12, v[14:15]
	v_lshl_add_u64 v[6:7], s[26:27], 0, v[6:7]
	v_lshl_add_u64 v[14:15], v[6:7], 0, v[18:19]
	v_mov_b32_e32 v8, v235
	v_mul_f32_e32 v6, 0x3c000000, v8
	v_pk_mul_f32 v[8:9], v[112:113], v[6:7] op_sel_hi:[1,0]
	v_pk_mul_f32 v[10:11], v[110:111], v[6:7] op_sel_hi:[1,0]
	v_pk_mul_f32 v[12:13], v[108:109], v[6:7] op_sel_hi:[1,0]
	v_pk_mul_f32 v[16:17], v[106:107], v[6:7] op_sel_hi:[1,0]
	v_pk_mul_f32 v[18:19], v[92:93], v[6:7] op_sel_hi:[1,0]
	v_pk_mul_f32 v[20:21], v[90:91], v[6:7] op_sel_hi:[1,0]
	v_pk_mul_f32 v[22:23], v[84:85], v[6:7] op_sel_hi:[1,0]
	v_pk_mul_f32 v[24:25], v[82:83], v[6:7] op_sel_hi:[1,0]
	v_cvt_pk_bf16_f32 v6, v10, v11
	v_cvt_pk_bf16_f32 v7, v8, v9
	v_cvt_pk_bf16_f32 v8, v16, v17
	v_cvt_pk_bf16_f32 v9, v12, v13
	v_cvt_pk_bf16_f32 v10, v20, v21
	v_cvt_pk_bf16_f32 v11, v18, v19
	v_cvt_pk_bf16_f32 v12, v24, v25
	v_cvt_pk_bf16_f32 v13, v22, v23
	global_store_dwordx4 v[14:15], v[6:9], off
	global_store_dwordx4 v[14:15], v[10:13], off offset:256
	v_add_co_u32_e32 v16, vcc, s4, v4
	v_lshl_add_u64 v[14:15], v[4:5], 0, s[14:15]
	s_nop 0
	v_addc_co_u32_e32 v17, vcc, 0, v5, vcc
	v_mov_b32_e32 v6, v236
	v_mul_f32_e32 v6, 0x3c000000, v6
	v_pk_mul_f32 v[8:9], v[104:105], v[6:7] op_sel_hi:[1,0]
	v_pk_mul_f32 v[10:11], v[102:103], v[6:7] op_sel_hi:[1,0]
	v_pk_mul_f32 v[12:13], v[100:101], v[6:7] op_sel_hi:[1,0]
	v_pk_mul_f32 v[18:19], v[98:99], v[6:7] op_sel_hi:[1,0]
	v_pk_mul_f32 v[20:21], v[96:97], v[6:7] op_sel_hi:[1,0]
	v_pk_mul_f32 v[22:23], v[94:95], v[6:7] op_sel_hi:[1,0]
	v_pk_mul_f32 v[24:25], v[88:89], v[6:7] op_sel_hi:[1,0]
	v_pk_mul_f32 v[26:27], v[86:87], v[6:7] op_sel_hi:[1,0]
	v_cvt_pk_bf16_f32 v6, v10, v11
	v_cvt_pk_bf16_f32 v7, v8, v9
	v_cvt_pk_bf16_f32 v8, v18, v19
	v_cvt_pk_bf16_f32 v9, v12, v13
	v_cvt_pk_bf16_f32 v10, v22, v23
	v_cvt_pk_bf16_f32 v11, v20, v21
	v_cvt_pk_bf16_f32 v12, v26, v27
	v_cvt_pk_bf16_f32 v13, v24, v25
	global_store_dwordx4 v[16:17], v[6:9], off
	global_store_dwordx4 v[14:15], v[10:13], off offset:256
	v_add_co_u32_e32 v16, vcc, s69, v4
	v_lshl_add_u64 v[14:15], v[4:5], 0, s[16:17]
	s_nop 0
	v_addc_co_u32_e32 v17, vcc, 0, v5, vcc
	v_mov_b32_e32 v6, v237
	v_mul_f32_e32 v6, 0x3c000000, v6
	v_pk_mul_f32 v[8:9], v[80:81], v[6:7] op_sel_hi:[1,0]
	v_pk_mul_f32 v[10:11], v[78:79], v[6:7] op_sel_hi:[1,0]
	v_pk_mul_f32 v[12:13], v[76:77], v[6:7] op_sel_hi:[1,0]
	v_pk_mul_f32 v[18:19], v[74:75], v[6:7] op_sel_hi:[1,0]
	v_pk_mul_f32 v[20:21], v[72:73], v[6:7] op_sel_hi:[1,0]
	v_pk_mul_f32 v[22:23], v[70:71], v[6:7] op_sel_hi:[1,0]
	v_pk_mul_f32 v[24:25], v[68:69], v[6:7] op_sel_hi:[1,0]
	v_pk_mul_f32 v[26:27], v[66:67], v[6:7] op_sel_hi:[1,0]
	v_cvt_pk_bf16_f32 v6, v10, v11
	v_cvt_pk_bf16_f32 v7, v8, v9
	v_cvt_pk_bf16_f32 v8, v18, v19
	v_cvt_pk_bf16_f32 v9, v12, v13
	v_cvt_pk_bf16_f32 v10, v22, v23
	v_cvt_pk_bf16_f32 v11, v20, v21
	v_cvt_pk_bf16_f32 v12, v26, v27
	v_cvt_pk_bf16_f32 v13, v24, v25
	global_store_dwordx4 v[16:17], v[6:9], off
	global_store_dwordx4 v[14:15], v[10:13], off offset:256
	v_add_co_u32_e32 v16, vcc, s70, v4
	v_lshl_add_u64 v[14:15], v[4:5], 0, s[18:19]
	s_nop 0
	v_addc_co_u32_e32 v17, vcc, 0, v5, vcc
	s_andn2_b64 vcc, exec, s[2:3]
	v_mov_b32_e32 v6, v238
	v_mul_f32_e32 v6, 0x3c000000, v6
	v_pk_mul_f32 v[8:9], v[64:65], v[6:7] op_sel_hi:[1,0]
	v_pk_mul_f32 v[10:11], v[62:63], v[6:7] op_sel_hi:[1,0]
	v_pk_mul_f32 v[12:13], v[60:61], v[6:7] op_sel_hi:[1,0]
	v_pk_mul_f32 v[18:19], v[58:59], v[6:7] op_sel_hi:[1,0]
	v_pk_mul_f32 v[20:21], v[56:57], v[6:7] op_sel_hi:[1,0]
	v_pk_mul_f32 v[22:23], v[54:55], v[6:7] op_sel_hi:[1,0]
	v_pk_mul_f32 v[24:25], v[52:53], v[6:7] op_sel_hi:[1,0]
	v_pk_mul_f32 v[26:27], v[50:51], v[6:7] op_sel_hi:[1,0]
	v_cvt_pk_bf16_f32 v6, v10, v11
	v_cvt_pk_bf16_f32 v7, v8, v9
	v_cvt_pk_bf16_f32 v8, v18, v19
	v_cvt_pk_bf16_f32 v9, v12, v13
	v_cvt_pk_bf16_f32 v10, v22, v23
	v_cvt_pk_bf16_f32 v11, v20, v21
	v_cvt_pk_bf16_f32 v12, v26, v27
	v_cvt_pk_bf16_f32 v13, v24, v25
	global_store_dwordx4 v[16:17], v[6:9], off
	global_store_dwordx4 v[14:15], v[10:13], off offset:256
	v_mov_b32_e32 v2, v239
	v_mul_f32_e32 v2, 0x3c000000, v2
	v_add_co_u32_e64 v12, s[0:1], s71, v4
	v_lshl_add_u64 v[10:11], v[4:5], 0, s[24:25]
	s_nop 0
	v_addc_co_u32_e64 v13, s[0:1], 0, v5, s[0:1]
	v_pk_mul_f32 v[4:5], v[48:49], v[2:3] op_sel_hi:[1,0]
	v_pk_mul_f32 v[6:7], v[46:47], v[2:3] op_sel_hi:[1,0]
	v_pk_mul_f32 v[8:9], v[44:45], v[2:3] op_sel_hi:[1,0]
	v_pk_mul_f32 v[14:15], v[42:43], v[2:3] op_sel_hi:[1,0]
	v_pk_mul_f32 v[16:17], v[40:41], v[2:3] op_sel_hi:[1,0]
	v_pk_mul_f32 v[18:19], v[38:39], v[2:3] op_sel_hi:[1,0]
	v_pk_mul_f32 v[20:21], v[36:37], v[2:3] op_sel_hi:[1,0]
	v_pk_mul_f32 v[22:23], v[34:35], v[2:3] op_sel_hi:[1,0]
	v_cvt_pk_bf16_f32 v2, v6, v7
	v_cvt_pk_bf16_f32 v3, v4, v5
	v_cvt_pk_bf16_f32 v4, v14, v15
	v_cvt_pk_bf16_f32 v5, v8, v9
	s_mov_b64 s[0:1], -1
	v_cvt_pk_bf16_f32 v6, v18, v19
	v_cvt_pk_bf16_f32 v7, v16, v17
	v_cvt_pk_bf16_f32 v8, v22, v23
	v_cvt_pk_bf16_f32 v9, v20, v21
	global_store_dwordx4 v[12:13], v[2:5], off
	global_store_dwordx4 v[10:11], v[6:9], off offset:256
	s_cbranch_vccnz .LBB0_1595
	s_andn2_b64 vcc, exec, s[6:7]
	s_cbranch_vccnz .LBB0_1594
	s_barrier
	s_branch .LBB0_1594
